# fp8 GEMM K-loops: the MFMA wave raises its priority in front of the barrier that opens its MFMA block instead of behind it
# baseline (speedup 1.0000x reference)
.LBB0_258:
	s_lshl_b64 s[2:3], s[82:83], 7
	s_add_u32 s26, s4, s2
	v_mov_b32_e32 v2, v184
	v_readfirstlane_b32 s28, v187
	ds_read_b128 v[218:221], v214 offset:16384
	ds_read_b128 v[222:225], v214 offset:17408
	ds_read_b128 v[226:229], v215 offset:16384
	ds_read_b128 v[230:233], v215 offset:17408
	ds_read_b128 v[234:237], v216 offset:16384
	ds_read_b128 v[238:241], v216 offset:17408
	ds_read_b128 v[242:245], v217 offset:16384
	ds_read_b128 v[246:249], v217 offset:17408
	s_addc_u32 s27, s5, s3
	s_mov_b32 m0, s28
	s_add_u32 s28, s26, 0x10000
	global_load_lds_dwordx4 v2, s[26:27]
	v_mov_b32_e32 v2, v184
	v_readfirstlane_b32 s30, v188
	s_addc_u32 s29, s27, 0
	s_mov_b32 m0, s30
	v_readfirstlane_b32 s30, v189
	global_load_lds_dwordx4 v2, s[28:29]
	s_add_u32 s28, s26, 0x20000
	v_mov_b32_e32 v2, v184
	s_addc_u32 s29, s27, 0
	s_mov_b32 m0, s30
	s_add_u32 s26, s26, 0x30000
	global_load_lds_dwordx4 v2, s[28:29]
	v_mov_b32_e32 v2, v184
	v_readfirstlane_b32 s28, v190
	s_addc_u32 s27, s27, 0
	s_mov_b32 m0, s28
	s_add_u32 s2, s6, s2
	global_load_lds_dwordx4 v2, s[26:27]
	v_mov_b32_e32 v2, v180
	v_readfirstlane_b32 s26, v191
	s_addc_u32 s3, s7, s3
	s_mov_b32 m0, s26
	v_readfirstlane_b32 s26, v201
	global_load_lds_dwordx4 v2, s[2:3]
	v_mov_b32_e32 v2, v181
	s_mov_b32 m0, s26
	s_nop 0
	global_load_lds_dwordx4 v2, s[2:3]
	s_waitcnt vmcnt(8)
	s_waitcnt lgkmcnt(0)
	s_setprio 1
	s_barrier
	s_waitcnt lgkmcnt(0)
	v_mfma_scale_f32_16x16x128_f8f6f4 v[144:147], v[20:27], v[218:225], v[144:147], v186, v185 op_sel_hi:[0,0,0]
	v_mfma_scale_f32_16x16x128_f8f6f4 v[140:143], v[28:35], v[218:225], v[140:143], v186, v185 op_sel_hi:[0,0,0]
	v_mfma_scale_f32_16x16x128_f8f6f4 v[136:139], v[20:27], v[226:233], v[136:139], v186, v185 op_sel_hi:[0,0,0]
	v_mfma_scale_f32_16x16x128_f8f6f4 v[132:135], v[28:35], v[226:233], v[132:135], v186, v185 op_sel_hi:[0,0,0]
	v_mfma_scale_f32_16x16x128_f8f6f4 v[128:131], v[20:27], v[234:241], v[128:131], v186, v185 op_sel_hi:[0,0,0]
	v_mfma_scale_f32_16x16x128_f8f6f4 v[124:127], v[28:35], v[234:241], v[124:127], v186, v185 op_sel_hi:[0,0,0]
	v_mfma_scale_f32_16x16x128_f8f6f4 v[120:123], v[20:27], v[242:249], v[120:123], v186, v185 op_sel_hi:[0,0,0]
	v_mfma_scale_f32_16x16x128_f8f6f4 v[116:119], v[28:35], v[242:249], v[116:119], v186, v185 op_sel_hi:[0,0,0]
	s_setprio 0
	s_setprio 1
	v_mfma_scale_f32_16x16x128_f8f6f4 v[80:83], v[4:11], v[218:225], v[80:83], v186, v185 op_sel_hi:[0,0,0]
	v_mfma_scale_f32_16x16x128_f8f6f4 v[76:79], v[12:19], v[218:225], v[76:79], v186, v185 op_sel_hi:[0,0,0]
	v_mfma_scale_f32_16x16x128_f8f6f4 v[72:75], v[4:11], v[226:233], v[72:75], v186, v185 op_sel_hi:[0,0,0]
	v_mfma_scale_f32_16x16x128_f8f6f4 v[68:71], v[12:19], v[226:233], v[68:71], v186, v185 op_sel_hi:[0,0,0]
	v_mfma_scale_f32_16x16x128_f8f6f4 v[64:67], v[4:11], v[234:241], v[64:67], v186, v185 op_sel_hi:[0,0,0]
	v_mfma_scale_f32_16x16x128_f8f6f4 v[60:63], v[12:19], v[234:241], v[60:63], v186, v185 op_sel_hi:[0,0,0]
	v_mfma_scale_f32_16x16x128_f8f6f4 v[56:59], v[4:11], v[242:249], v[56:59], v186, v185 op_sel_hi:[0,0,0]
	v_mfma_scale_f32_16x16x128_f8f6f4 v[52:55], v[12:19], v[242:249], v[52:55], v186, v185 op_sel_hi:[0,0,0]
	s_setprio 0
	s_barrier
	ds_read_b128 v[20:23], v212
	ds_read_b128 v[24:27], v212 offset:1024
	ds_read_b128 v[28:31], v212 offset:2048
	ds_read_b128 v[32:35], v212 offset:3072
	ds_read_b128 v[4:7], v213
	ds_read_b128 v[8:11], v213 offset:1024
	ds_read_b128 v[12:15], v213 offset:2048
	ds_read_b128 v[16:19], v213 offset:3072
	v_mov_b32_e32 v2, v182
	v_readfirstlane_b32 s26, v202
	ds_read_b128 v[218:221], v214 offset:32768
	ds_read_b128 v[222:225], v214 offset:33792
	ds_read_b128 v[226:229], v215 offset:32768
	ds_read_b128 v[230:233], v215 offset:33792
	ds_read_b128 v[234:237], v216 offset:32768
	ds_read_b128 v[238:241], v216 offset:33792
	ds_read_b128 v[242:245], v217 offset:32768
	ds_read_b128 v[246:249], v217 offset:33792
	s_mov_b32 m0, s26
	v_readfirstlane_b32 s26, v203
	global_load_lds_dwordx4 v2, s[2:3]
	v_mov_b32_e32 v2, v183
	s_mov_b32 m0, s26
	s_nop 0
	global_load_lds_dwordx4 v2, s[2:3]
	s_waitcnt vmcnt(8)
	s_waitcnt lgkmcnt(0)
	s_setprio 1
	s_barrier
	s_waitcnt lgkmcnt(0)
	v_mfma_scale_f32_16x16x128_f8f6f4 v[176:179], v[20:27], v[218:225], v[176:179], v186, v185 op_sel_hi:[0,0,0]
	v_mfma_scale_f32_16x16x128_f8f6f4 v[172:175], v[28:35], v[218:225], v[172:175], v186, v185 op_sel_hi:[0,0,0]
	v_mfma_scale_f32_16x16x128_f8f6f4 v[168:171], v[20:27], v[226:233], v[168:171], v186, v185 op_sel_hi:[0,0,0]
	v_mfma_scale_f32_16x16x128_f8f6f4 v[164:167], v[28:35], v[226:233], v[164:167], v186, v185 op_sel_hi:[0,0,0]
	v_mfma_scale_f32_16x16x128_f8f6f4 v[160:163], v[20:27], v[234:241], v[160:163], v186, v185 op_sel_hi:[0,0,0]
	v_mfma_scale_f32_16x16x128_f8f6f4 v[156:159], v[28:35], v[234:241], v[156:159], v186, v185 op_sel_hi:[0,0,0]
	v_mfma_scale_f32_16x16x128_f8f6f4 v[152:155], v[20:27], v[242:249], v[152:155], v186, v185 op_sel_hi:[0,0,0]
	v_mfma_scale_f32_16x16x128_f8f6f4 v[148:151], v[28:35], v[242:249], v[148:151], v186, v185 op_sel_hi:[0,0,0]
	s_setprio 0
	s_setprio 1
	v_mfma_scale_f32_16x16x128_f8f6f4 v[112:115], v[4:11], v[218:225], v[112:115], v186, v185 op_sel_hi:[0,0,0]
	v_mfma_scale_f32_16x16x128_f8f6f4 v[108:111], v[12:19], v[218:225], v[108:111], v186, v185 op_sel_hi:[0,0,0]
	v_mfma_scale_f32_16x16x128_f8f6f4 v[104:107], v[4:11], v[226:233], v[104:107], v186, v185 op_sel_hi:[0,0,0]
	v_mfma_scale_f32_16x16x128_f8f6f4 v[100:103], v[12:19], v[226:233], v[100:103], v186, v185 op_sel_hi:[0,0,0]
	v_mfma_scale_f32_16x16x128_f8f6f4 v[96:99], v[4:11], v[234:241], v[96:99], v186, v185 op_sel_hi:[0,0,0]
	v_mfma_scale_f32_16x16x128_f8f6f4 v[92:95], v[12:19], v[234:241], v[92:95], v186, v185 op_sel_hi:[0,0,0]
	v_mfma_scale_f32_16x16x128_f8f6f4 v[88:91], v[4:11], v[242:249], v[88:91], v186, v185 op_sel_hi:[0,0,0]
	v_mfma_scale_f32_16x16x128_f8f6f4 v[84:87], v[12:19], v[242:249], v[84:87], v186, v185 op_sel_hi:[0,0,0]
	s_setprio 0
	s_barrier
	s_add_i32 s82, s82, 1
	s_lshl_b64 s[2:3], s[82:83], 7
	s_add_u32 s26, s4, s2
	v_mov_b32_e32 v2, v184
	v_readfirstlane_b32 s28, v204
	ds_read_b128 v[218:221], v214 offset:49152
	ds_read_b128 v[222:225], v214 offset:50176
	ds_read_b128 v[226:229], v215 offset:49152
	ds_read_b128 v[230:233], v215 offset:50176
	ds_read_b128 v[234:237], v216 offset:49152
	ds_read_b128 v[238:241], v216 offset:50176
	ds_read_b128 v[242:245], v217 offset:49152
	ds_read_b128 v[246:249], v217 offset:50176
	s_addc_u32 s27, s5, s3
	s_mov_b32 m0, s28
	s_add_u32 s28, s26, 0x10000
	global_load_lds_dwordx4 v2, s[26:27]
	v_mov_b32_e32 v2, v184
	v_readfirstlane_b32 s30, v205
	s_addc_u32 s29, s27, 0
	s_mov_b32 m0, s30
	v_readfirstlane_b32 s30, v208
	global_load_lds_dwordx4 v2, s[28:29]
	s_add_u32 s28, s26, 0x20000
	v_mov_b32_e32 v2, v184
	s_addc_u32 s29, s27, 0
	s_mov_b32 m0, s30
	s_add_u32 s26, s26, 0x30000
	global_load_lds_dwordx4 v2, s[28:29]
	v_mov_b32_e32 v2, v184
	v_readfirstlane_b32 s28, v209
	s_addc_u32 s27, s27, 0
	s_mov_b32 m0, s28
	s_add_u32 s2, s6, s2
	global_load_lds_dwordx4 v2, s[26:27]
	v_mov_b32_e32 v2, v180
	v_readfirstlane_b32 s26, v206
	s_addc_u32 s3, s7, s3
	s_mov_b32 m0, s26
	v_readfirstlane_b32 s26, v207
	global_load_lds_dwordx4 v2, s[2:3]
	v_mov_b32_e32 v2, v181
	s_mov_b32 m0, s26
	s_nop 0
	global_load_lds_dwordx4 v2, s[2:3]
	s_waitcnt vmcnt(8)
	s_waitcnt lgkmcnt(0)
	s_setprio 1
	s_barrier
	s_waitcnt lgkmcnt(0)
	v_mfma_scale_f32_16x16x128_f8f6f4 v[144:147], v[20:27], v[218:225], v[144:147], v186, v185 op_sel_hi:[0,0,0]
	v_mfma_scale_f32_16x16x128_f8f6f4 v[140:143], v[28:35], v[218:225], v[140:143], v186, v185 op_sel_hi:[0,0,0]
	v_mfma_scale_f32_16x16x128_f8f6f4 v[136:139], v[20:27], v[226:233], v[136:139], v186, v185 op_sel_hi:[0,0,0]
	v_mfma_scale_f32_16x16x128_f8f6f4 v[132:135], v[28:35], v[226:233], v[132:135], v186, v185 op_sel_hi:[0,0,0]
	v_mfma_scale_f32_16x16x128_f8f6f4 v[128:131], v[20:27], v[234:241], v[128:131], v186, v185 op_sel_hi:[0,0,0]
	v_mfma_scale_f32_16x16x128_f8f6f4 v[124:127], v[28:35], v[234:241], v[124:127], v186, v185 op_sel_hi:[0,0,0]
	v_mfma_scale_f32_16x16x128_f8f6f4 v[120:123], v[20:27], v[242:249], v[120:123], v186, v185 op_sel_hi:[0,0,0]
	v_mfma_scale_f32_16x16x128_f8f6f4 v[116:119], v[28:35], v[242:249], v[116:119], v186, v185 op_sel_hi:[0,0,0]
	s_setprio 0
	s_setprio 1
	v_mfma_scale_f32_16x16x128_f8f6f4 v[80:83], v[4:11], v[218:225], v[80:83], v186, v185 op_sel_hi:[0,0,0]
	v_mfma_scale_f32_16x16x128_f8f6f4 v[76:79], v[12:19], v[218:225], v[76:79], v186, v185 op_sel_hi:[0,0,0]
	v_mfma_scale_f32_16x16x128_f8f6f4 v[72:75], v[4:11], v[226:233], v[72:75], v186, v185 op_sel_hi:[0,0,0]
	v_mfma_scale_f32_16x16x128_f8f6f4 v[68:71], v[12:19], v[226:233], v[68:71], v186, v185 op_sel_hi:[0,0,0]
	v_mfma_scale_f32_16x16x128_f8f6f4 v[64:67], v[4:11], v[234:241], v[64:67], v186, v185 op_sel_hi:[0,0,0]
	v_mfma_scale_f32_16x16x128_f8f6f4 v[60:63], v[12:19], v[234:241], v[60:63], v186, v185 op_sel_hi:[0,0,0]
	v_mfma_scale_f32_16x16x128_f8f6f4 v[56:59], v[4:11], v[242:249], v[56:59], v186, v185 op_sel_hi:[0,0,0]
	v_mfma_scale_f32_16x16x128_f8f6f4 v[52:55], v[12:19], v[242:249], v[52:55], v186, v185 op_sel_hi:[0,0,0]
	s_setprio 0
	s_barrier
	s_add_i32 s25, s25, 2
	s_add_u32 s12, s12, 0x100
	s_addc_u32 s13, s13, 0
	s_cmp_gt_u32 s25, 5
	s_cbranch_scc1 .LBB0_263
.LBB0_259:
	ds_read_b128 v[20:23], v210
	ds_read_b128 v[24:27], v210 offset:1024
	ds_read_b128 v[28:31], v210 offset:2048
	ds_read_b128 v[32:35], v210 offset:3072
	ds_read_b128 v[4:7], v211
	ds_read_b128 v[8:11], v211 offset:1024
	ds_read_b128 v[12:15], v211 offset:2048
	ds_read_b128 v[16:19], v211 offset:3072
	s_add_u32 s2, s6, s12
	s_addc_u32 s3, s7, s13
	v_add_u32_e32 v192, 0xc000, v191
	s_add_u32 s2, s2, 0x80
	v_mov_b32_e32 v2, v182
	v_readfirstlane_b32 s26, v192
	v_add_u32_e32 v192, 0xe000, v191
	ds_read_b128 v[218:221], v214
	ds_read_b128 v[222:225], v214 offset:1024
	ds_read_b128 v[226:229], v215
	ds_read_b128 v[230:233], v215 offset:1024
	ds_read_b128 v[234:237], v216
	ds_read_b128 v[238:241], v216 offset:1024
	ds_read_b128 v[242:245], v217
	ds_read_b128 v[246:249], v217 offset:1024
	s_addc_u32 s3, s3, 0
	s_mov_b32 m0, s26
	v_readfirstlane_b32 s26, v192
	global_load_lds_dwordx4 v2, s[2:3]
	v_mov_b32_e32 v2, v183
	s_mov_b32 m0, s26
	s_nop 0
	global_load_lds_dwordx4 v2, s[2:3]
	s_waitcnt vmcnt(8)
	s_waitcnt lgkmcnt(0)
	s_setprio 1
	s_barrier
	s_waitcnt lgkmcnt(0)
	v_mfma_scale_f32_16x16x128_f8f6f4 v[176:179], v[20:27], v[218:225], v[176:179], v186, v185 op_sel_hi:[0,0,0]
	v_mfma_scale_f32_16x16x128_f8f6f4 v[172:175], v[28:35], v[218:225], v[172:175], v186, v185 op_sel_hi:[0,0,0]
	v_mfma_scale_f32_16x16x128_f8f6f4 v[168:171], v[20:27], v[226:233], v[168:171], v186, v185 op_sel_hi:[0,0,0]
	v_mfma_scale_f32_16x16x128_f8f6f4 v[164:167], v[28:35], v[226:233], v[164:167], v186, v185 op_sel_hi:[0,0,0]
	v_mfma_scale_f32_16x16x128_f8f6f4 v[160:163], v[20:27], v[234:241], v[160:163], v186, v185 op_sel_hi:[0,0,0]
	v_mfma_scale_f32_16x16x128_f8f6f4 v[156:159], v[28:35], v[234:241], v[156:159], v186, v185 op_sel_hi:[0,0,0]
	v_mfma_scale_f32_16x16x128_f8f6f4 v[152:155], v[20:27], v[242:249], v[152:155], v186, v185 op_sel_hi:[0,0,0]
	v_mfma_scale_f32_16x16x128_f8f6f4 v[148:151], v[28:35], v[242:249], v[148:151], v186, v185 op_sel_hi:[0,0,0]
	s_setprio 0
	s_setprio 1
	v_mfma_scale_f32_16x16x128_f8f6f4 v[112:115], v[4:11], v[218:225], v[112:115], v186, v185 op_sel_hi:[0,0,0]
	v_mfma_scale_f32_16x16x128_f8f6f4 v[108:111], v[12:19], v[218:225], v[108:111], v186, v185 op_sel_hi:[0,0,0]
	v_mfma_scale_f32_16x16x128_f8f6f4 v[104:107], v[4:11], v[226:233], v[104:107], v186, v185 op_sel_hi:[0,0,0]
	v_mfma_scale_f32_16x16x128_f8f6f4 v[100:103], v[12:19], v[226:233], v[100:103], v186, v185 op_sel_hi:[0,0,0]
	v_mfma_scale_f32_16x16x128_f8f6f4 v[96:99], v[4:11], v[234:241], v[96:99], v186, v185 op_sel_hi:[0,0,0]
	v_mfma_scale_f32_16x16x128_f8f6f4 v[92:95], v[12:19], v[234:241], v[92:95], v186, v185 op_sel_hi:[0,0,0]
	v_mfma_scale_f32_16x16x128_f8f6f4 v[88:91], v[4:11], v[242:249], v[88:91], v186, v185 op_sel_hi:[0,0,0]
	v_mfma_scale_f32_16x16x128_f8f6f4 v[84:87], v[12:19], v[242:249], v[84:87], v186, v185 op_sel_hi:[0,0,0]
	s_cmp_lg_u32 s25, 4
	s_setprio 0
	s_barrier
	s_cbranch_scc1 .LBB0_262
	s_cmpk_gt_u32 s15, 0xd7f
	s_mov_b64 s[20:21], 0
	s_cbranch_scc1 .LBB0_257
	v_readlane_b32 s2, v255, 41
	v_readlane_b32 s4, v255, 40
	v_mov_b32_e32 v2, v0
	s_mov_b64 s[20:21], -1
	v_ashrrev_i32_e32 v181, 31, v2
	v_lshrrev_b32_e32 v181, 26, v181
	v_lshlrev_b32_e32 v180, 4, v2
	v_add_u32_e32 v181, v2, v181
	v_bfe_i32 v2, v2, 27, 1
	s_waitcnt lgkmcnt(0)
	s_lshr_b32 s2, s2, 16
	v_lshrrev_b32_e32 v2, 22, v2
	s_cmp_lg_u32 s2, 0
	v_add_u32_e32 v2, v180, v2
	s_cselect_b64 s[2:3], -1, 0
	v_and_b32_e32 v2, 0xfffffc00, v2
	s_cmp_lg_u64 s[2:3], 0
	v_sub_u32_e32 v2, v180, v2
	s_addc_u32 s16, s4, s15
	s_lshr_b32 s3, s15, 3
	v_lshrrev_b32_e32 v180, 4, v2
	s_and_b32 s2, s15, 7
	s_add_i32 s4, s3, 0xffffff28
	v_bitop3_b32 v2, v180, v2, 32 bitop3:0x6c
	s_cmpk_lt_u32 s15, 0x6c0
	v_ashrrev_i32_e32 v182, 31, v2
	s_cselect_b32 s3, s3, s4
	s_cmpk_gt_u32 s15, 0x6bf
	v_lshrrev_b32_e32 v182, 26, v182
	s_cselect_b32 s4, 8, 0
	s_and_b32 s5, s3, 7
	v_add_u32_e32 v182, v2, v182
	s_or_b32 s4, s5, s4
	v_lshrrev_b32_e32 v183, 6, v182
	v_and_b32_e32 v182, 0xc0, v182
	s_lshr_b32 s82, s3, 3
	s_lshl_b32 s3, s4, 3
	v_ashrrev_i32_e32 v181, 6, v181
	v_sub_u32_e32 v2, v2, v182
	s_or_b32 s14, s3, s2
	v_lshlrev_b32_e32 v180, 3, v181
	v_lshlrev_b32_e32 v181, 5, v181
	v_ashrrev_i16_sdwa v2, v196, sext(v2) dst_sel:DWORD dst_unused:UNUSED_PAD src0_sel:DWORD src1_sel:BYTE_0
	s_lshl_b64 s[2:3], s[82:83], 18
	v_and_b32_e32 v180, 0x3ffff0, v180
	v_and_b32_e32 v181, 32, v181
	v_bfe_i32 v2, v2, 0, 16
	s_add_u32 s4, s19, s2
	s_addc_u32 s5, s22, s3
	s_lshl_b32 s2, s14, 18
	v_add_lshl_u32 v180, v183, v180, 10
	v_add_lshl_u32 v2, v181, v2, 1
	v_add3_u32 v180, v180, s2, v2
	v_add_u32_e32 v181, 0x10000, v180
	v_add_u32_e32 v182, 0x20000, v180
	v_add_u32_e32 v183, 0x30000, v180
	s_mov_b64 s[6:7], s[8:9]
	s_mov_b32 s15, s16
	s_mov_b32 s16, s82
	s_branch .LBB0_257

.LBB0_902:
	ds_read_b128 v[20:23], v186
	ds_read_b128 v[24:27], v186 offset:1024
	ds_read_b128 v[28:31], v186 offset:2048
	ds_read_b128 v[32:35], v186 offset:3072
	ds_read_b128 v[4:7], v187
	ds_read_b128 v[8:11], v187 offset:1024
	ds_read_b128 v[12:15], v187 offset:2048
	ds_read_b128 v[16:19], v187 offset:3072
	v_add_u32_e32 v165, 0xc000, v172
	s_add_u32 s2, s34, 0x80
	v_mov_b32_e32 v164, v176
	v_readfirstlane_b32 s13, v165
	v_add_u32_e32 v165, 0xe000, v172
	ds_read_b128 v[204:207], v188
	ds_read_b128 v[208:211], v188 offset:1024
	ds_read_b128 v[212:215], v189
	ds_read_b128 v[216:219], v189 offset:1024
	ds_read_b128 v[220:223], v190
	ds_read_b128 v[224:227], v190 offset:1024
	ds_read_b128 v[228:231], v191
	ds_read_b128 v[232:235], v191 offset:1024
	s_addc_u32 s3, s35, 0
	s_mov_b32 m0, s13
	v_readfirstlane_b32 s12, v165
	global_load_lds_dwordx4 v164, s[2:3]
	v_mov_b32_e32 v164, v178
	s_mov_b32 m0, s12
	s_nop 0
	global_load_lds_dwordx4 v164, s[2:3]
	s_waitcnt vmcnt(8)
	s_waitcnt lgkmcnt(0)
	s_setprio 1
	s_barrier
	s_waitcnt lgkmcnt(0)
	v_mfma_scale_f32_16x16x128_f8f6f4 v[160:163], v[20:27], v[204:211], v[160:163], v166, v167 op_sel_hi:[0,0,0]
	v_mfma_scale_f32_16x16x128_f8f6f4 v[156:159], v[28:35], v[204:211], v[156:159], v166, v167 op_sel_hi:[0,0,0]
	v_mfma_scale_f32_16x16x128_f8f6f4 v[152:155], v[20:27], v[212:219], v[152:155], v166, v167 op_sel_hi:[0,0,0]
	v_mfma_scale_f32_16x16x128_f8f6f4 v[148:151], v[28:35], v[212:219], v[148:151], v166, v167 op_sel_hi:[0,0,0]
	v_mfma_scale_f32_16x16x128_f8f6f4 v[144:147], v[20:27], v[220:227], v[144:147], v166, v167 op_sel_hi:[0,0,0]
	v_mfma_scale_f32_16x16x128_f8f6f4 v[140:143], v[28:35], v[220:227], v[140:143], v166, v167 op_sel_hi:[0,0,0]
	v_mfma_scale_f32_16x16x128_f8f6f4 v[136:139], v[20:27], v[228:235], v[136:139], v166, v167 op_sel_hi:[0,0,0]
	v_mfma_scale_f32_16x16x128_f8f6f4 v[132:135], v[28:35], v[228:235], v[132:135], v166, v167 op_sel_hi:[0,0,0]
	s_setprio 0
	s_setprio 1
	v_mfma_scale_f32_16x16x128_f8f6f4 v[128:131], v[4:11], v[204:211], v[128:131], v166, v167 op_sel_hi:[0,0,0]
	v_mfma_scale_f32_16x16x128_f8f6f4 v[124:127], v[12:19], v[204:211], v[124:127], v166, v167 op_sel_hi:[0,0,0]
	v_mfma_scale_f32_16x16x128_f8f6f4 v[120:123], v[4:11], v[212:219], v[120:123], v166, v167 op_sel_hi:[0,0,0]
	v_mfma_scale_f32_16x16x128_f8f6f4 v[116:119], v[12:19], v[212:219], v[116:119], v166, v167 op_sel_hi:[0,0,0]
	v_mfma_scale_f32_16x16x128_f8f6f4 v[112:115], v[4:11], v[220:227], v[112:115], v166, v167 op_sel_hi:[0,0,0]
	v_mfma_scale_f32_16x16x128_f8f6f4 v[108:111], v[12:19], v[220:227], v[108:111], v166, v167 op_sel_hi:[0,0,0]
	v_mfma_scale_f32_16x16x128_f8f6f4 v[104:107], v[4:11], v[228:235], v[104:107], v166, v167 op_sel_hi:[0,0,0]
	v_mfma_scale_f32_16x16x128_f8f6f4 v[100:103], v[12:19], v[228:235], v[100:103], v166, v167 op_sel_hi:[0,0,0]
	s_setprio 0
	s_barrier
	s_add_u32 s2, s6, 0x100
	v_mov_b32_e32 v164, v2
	v_readfirstlane_b32 s23, v168
	ds_read_b128 v[204:207], v188 offset:16384
	ds_read_b128 v[208:211], v188 offset:17408
	ds_read_b128 v[212:215], v189 offset:16384
	ds_read_b128 v[216:219], v189 offset:17408
	ds_read_b128 v[220:223], v190 offset:16384
	ds_read_b128 v[224:227], v190 offset:17408
	ds_read_b128 v[228:231], v191 offset:16384
	ds_read_b128 v[232:235], v191 offset:17408
	s_addc_u32 s3, s7, 0
	s_mov_b32 m0, s23
	v_readfirstlane_b32 s23, v169
	global_load_lds_dwordx4 v164, s[2:3]
	s_add_u32 s2, s6, 0x8100
	v_mov_b32_e32 v164, v2
	s_addc_u32 s3, s7, 0
	s_mov_b32 m0, s23
	v_readfirstlane_b32 s23, v170
	global_load_lds_dwordx4 v164, s[2:3]
	s_add_u32 s2, s6, 0x10100
	v_mov_b32_e32 v164, v2
	s_addc_u32 s3, s7, 0
	s_mov_b32 m0, s23
	v_readfirstlane_b32 s23, v171
	global_load_lds_dwordx4 v164, s[2:3]
	s_add_u32 s2, s6, 0x18100
	v_mov_b32_e32 v164, v2
	s_addc_u32 s3, s7, 0
	s_mov_b32 m0, s23
	v_readfirstlane_b32 s23, v172
	global_load_lds_dwordx4 v164, s[2:3]
	s_add_u32 s2, s34, 0x100
	v_mov_b32_e32 v164, v173
	s_addc_u32 s3, s35, 0
	s_mov_b32 m0, s23
	v_readfirstlane_b32 s23, v174
	global_load_lds_dwordx4 v164, s[2:3]
	v_mov_b32_e32 v164, v175
	s_mov_b32 m0, s23
	s_nop 0
	global_load_lds_dwordx4 v164, s[2:3]
	s_waitcnt vmcnt(8)
	s_waitcnt lgkmcnt(0)
	s_setprio 1
	s_barrier
	s_waitcnt lgkmcnt(0)
	v_mfma_scale_f32_16x16x128_f8f6f4 v[96:99], v[20:27], v[204:211], v[96:99], v166, v167 op_sel_hi:[0,0,0]
	v_mfma_scale_f32_16x16x128_f8f6f4 v[92:95], v[28:35], v[204:211], v[92:95], v166, v167 op_sel_hi:[0,0,0]
	v_mfma_scale_f32_16x16x128_f8f6f4 v[88:91], v[20:27], v[212:219], v[88:91], v166, v167 op_sel_hi:[0,0,0]
	v_mfma_scale_f32_16x16x128_f8f6f4 v[84:87], v[28:35], v[212:219], v[84:87], v166, v167 op_sel_hi:[0,0,0]
	v_mfma_scale_f32_16x16x128_f8f6f4 v[80:83], v[20:27], v[220:227], v[80:83], v166, v167 op_sel_hi:[0,0,0]
	v_mfma_scale_f32_16x16x128_f8f6f4 v[76:79], v[28:35], v[220:227], v[76:79], v166, v167 op_sel_hi:[0,0,0]
	v_mfma_scale_f32_16x16x128_f8f6f4 v[72:75], v[20:27], v[228:235], v[72:75], v166, v167 op_sel_hi:[0,0,0]
	v_mfma_scale_f32_16x16x128_f8f6f4 v[68:71], v[28:35], v[228:235], v[68:71], v166, v167 op_sel_hi:[0,0,0]
	s_setprio 0
	s_setprio 1
	v_mfma_scale_f32_16x16x128_f8f6f4 v[64:67], v[4:11], v[204:211], v[64:67], v166, v167 op_sel_hi:[0,0,0]
	v_mfma_scale_f32_16x16x128_f8f6f4 v[60:63], v[12:19], v[204:211], v[60:63], v166, v167 op_sel_hi:[0,0,0]
	v_mfma_scale_f32_16x16x128_f8f6f4 v[56:59], v[4:11], v[212:219], v[56:59], v166, v167 op_sel_hi:[0,0,0]
	v_mfma_scale_f32_16x16x128_f8f6f4 v[52:55], v[12:19], v[212:219], v[52:55], v166, v167 op_sel_hi:[0,0,0]
	v_mfma_scale_f32_16x16x128_f8f6f4 v[48:51], v[4:11], v[220:227], v[48:51], v166, v167 op_sel_hi:[0,0,0]
	v_mfma_scale_f32_16x16x128_f8f6f4 v[44:47], v[12:19], v[220:227], v[44:47], v166, v167 op_sel_hi:[0,0,0]
	v_mfma_scale_f32_16x16x128_f8f6f4 v[40:43], v[4:11], v[228:235], v[40:43], v166, v167 op_sel_hi:[0,0,0]
	v_mfma_scale_f32_16x16x128_f8f6f4 v[36:39], v[12:19], v[228:235], v[36:39], v166, v167 op_sel_hi:[0,0,0]
	s_setprio 0
	s_barrier
	ds_read_b128 v[20:23], v201
	ds_read_b128 v[24:27], v201 offset:1024
	ds_read_b128 v[28:31], v201 offset:2048
	ds_read_b128 v[32:35], v201 offset:3072
	ds_read_b128 v[4:7], v202
	ds_read_b128 v[8:11], v202 offset:1024
	ds_read_b128 v[12:15], v202 offset:2048
	ds_read_b128 v[16:19], v202 offset:3072
	v_mov_b32_e32 v164, v176
	v_readfirstlane_b32 s23, v177
	ds_read_b128 v[204:207], v188 offset:32768
	ds_read_b128 v[208:211], v188 offset:33792
	ds_read_b128 v[212:215], v189 offset:32768
	ds_read_b128 v[216:219], v189 offset:33792
	ds_read_b128 v[220:223], v190 offset:32768
	ds_read_b128 v[224:227], v190 offset:33792
	ds_read_b128 v[228:231], v191 offset:32768
	ds_read_b128 v[232:235], v191 offset:33792
	s_mov_b32 m0, s23
	v_readfirstlane_b32 s23, v179
	global_load_lds_dwordx4 v164, s[2:3]
	v_mov_b32_e32 v164, v178
	s_mov_b32 m0, s23
	s_nop 0
	global_load_lds_dwordx4 v164, s[2:3]
	s_waitcnt vmcnt(8)
	s_waitcnt lgkmcnt(0)
	s_setprio 1
	s_barrier
	s_waitcnt lgkmcnt(0)
	v_mfma_scale_f32_16x16x128_f8f6f4 v[160:163], v[20:27], v[204:211], v[160:163], v166, v167 op_sel_hi:[0,0,0]
	v_mfma_scale_f32_16x16x128_f8f6f4 v[156:159], v[28:35], v[204:211], v[156:159], v166, v167 op_sel_hi:[0,0,0]
	v_mfma_scale_f32_16x16x128_f8f6f4 v[152:155], v[20:27], v[212:219], v[152:155], v166, v167 op_sel_hi:[0,0,0]
	v_mfma_scale_f32_16x16x128_f8f6f4 v[148:151], v[28:35], v[212:219], v[148:151], v166, v167 op_sel_hi:[0,0,0]
	v_mfma_scale_f32_16x16x128_f8f6f4 v[144:147], v[20:27], v[220:227], v[144:147], v166, v167 op_sel_hi:[0,0,0]
	v_mfma_scale_f32_16x16x128_f8f6f4 v[140:143], v[28:35], v[220:227], v[140:143], v166, v167 op_sel_hi:[0,0,0]
	v_mfma_scale_f32_16x16x128_f8f6f4 v[136:139], v[20:27], v[228:235], v[136:139], v166, v167 op_sel_hi:[0,0,0]
	v_mfma_scale_f32_16x16x128_f8f6f4 v[132:135], v[28:35], v[228:235], v[132:135], v166, v167 op_sel_hi:[0,0,0]
	s_setprio 0
	s_setprio 1
	v_mfma_scale_f32_16x16x128_f8f6f4 v[128:131], v[4:11], v[204:211], v[128:131], v166, v167 op_sel_hi:[0,0,0]
	v_mfma_scale_f32_16x16x128_f8f6f4 v[124:127], v[12:19], v[204:211], v[124:127], v166, v167 op_sel_hi:[0,0,0]
	v_mfma_scale_f32_16x16x128_f8f6f4 v[120:123], v[4:11], v[212:219], v[120:123], v166, v167 op_sel_hi:[0,0,0]
	v_mfma_scale_f32_16x16x128_f8f6f4 v[116:119], v[12:19], v[212:219], v[116:119], v166, v167 op_sel_hi:[0,0,0]
	v_mfma_scale_f32_16x16x128_f8f6f4 v[112:115], v[4:11], v[220:227], v[112:115], v166, v167 op_sel_hi:[0,0,0]
	v_mfma_scale_f32_16x16x128_f8f6f4 v[108:111], v[12:19], v[220:227], v[108:111], v166, v167 op_sel_hi:[0,0,0]
	v_mfma_scale_f32_16x16x128_f8f6f4 v[104:107], v[4:11], v[228:235], v[104:107], v166, v167 op_sel_hi:[0,0,0]
	v_mfma_scale_f32_16x16x128_f8f6f4 v[100:103], v[12:19], v[228:235], v[100:103], v166, v167 op_sel_hi:[0,0,0]
	s_setprio 0
	s_barrier
	s_add_u32 s2, s6, 0x180
	v_mov_b32_e32 v164, v2
	v_readfirstlane_b32 s23, v180
	ds_read_b128 v[204:207], v188 offset:49152
	ds_read_b128 v[208:211], v188 offset:50176
	ds_read_b128 v[212:215], v189 offset:49152
	ds_read_b128 v[216:219], v189 offset:50176
	ds_read_b128 v[220:223], v190 offset:49152
	ds_read_b128 v[224:227], v190 offset:50176
	ds_read_b128 v[228:231], v191 offset:49152
	ds_read_b128 v[232:235], v191 offset:50176
	s_addc_u32 s3, s7, 0
	s_mov_b32 m0, s23
	v_readfirstlane_b32 s23, v181
	global_load_lds_dwordx4 v164, s[2:3]
	s_add_u32 s2, s6, 0x8180
	v_mov_b32_e32 v164, v2
	s_addc_u32 s3, s7, 0
	s_mov_b32 m0, s23
	v_readfirstlane_b32 s23, v184
	global_load_lds_dwordx4 v164, s[2:3]
	s_add_u32 s2, s6, 0x10180
	v_mov_b32_e32 v164, v2
	s_addc_u32 s3, s7, 0
	s_mov_b32 m0, s23
	v_readfirstlane_b32 s23, v185
	global_load_lds_dwordx4 v164, s[2:3]
	s_add_u32 s2, s6, 0x18180
	v_mov_b32_e32 v164, v2
	s_addc_u32 s3, s7, 0
	s_mov_b32 m0, s23
	v_readfirstlane_b32 s23, v182
	global_load_lds_dwordx4 v164, s[2:3]
	s_add_u32 s2, s34, 0x180
	v_mov_b32_e32 v164, v173
	s_addc_u32 s3, s35, 0
	s_mov_b32 m0, s23
	v_readfirstlane_b32 s23, v183
	global_load_lds_dwordx4 v164, s[2:3]
	v_mov_b32_e32 v164, v175
	s_mov_b32 m0, s23
	s_nop 0
	global_load_lds_dwordx4 v164, s[2:3]
	s_waitcnt vmcnt(8)
	s_waitcnt lgkmcnt(0)
	s_setprio 1
	s_barrier
	s_waitcnt lgkmcnt(0)
	v_mfma_scale_f32_16x16x128_f8f6f4 v[96:99], v[20:27], v[204:211], v[96:99], v166, v167 op_sel_hi:[0,0,0]
	v_mfma_scale_f32_16x16x128_f8f6f4 v[92:95], v[28:35], v[204:211], v[92:95], v166, v167 op_sel_hi:[0,0,0]
	v_mfma_scale_f32_16x16x128_f8f6f4 v[88:91], v[20:27], v[212:219], v[88:91], v166, v167 op_sel_hi:[0,0,0]
	v_mfma_scale_f32_16x16x128_f8f6f4 v[84:87], v[28:35], v[212:219], v[84:87], v166, v167 op_sel_hi:[0,0,0]
	v_mfma_scale_f32_16x16x128_f8f6f4 v[80:83], v[20:27], v[220:227], v[80:83], v166, v167 op_sel_hi:[0,0,0]
	v_mfma_scale_f32_16x16x128_f8f6f4 v[76:79], v[28:35], v[220:227], v[76:79], v166, v167 op_sel_hi:[0,0,0]
	v_mfma_scale_f32_16x16x128_f8f6f4 v[72:75], v[20:27], v[228:235], v[72:75], v166, v167 op_sel_hi:[0,0,0]
	v_mfma_scale_f32_16x16x128_f8f6f4 v[68:71], v[28:35], v[228:235], v[68:71], v166, v167 op_sel_hi:[0,0,0]
	s_setprio 0
	s_setprio 1
	v_mfma_scale_f32_16x16x128_f8f6f4 v[64:67], v[4:11], v[204:211], v[64:67], v166, v167 op_sel_hi:[0,0,0]
	v_mfma_scale_f32_16x16x128_f8f6f4 v[60:63], v[12:19], v[204:211], v[60:63], v166, v167 op_sel_hi:[0,0,0]
	v_mfma_scale_f32_16x16x128_f8f6f4 v[56:59], v[4:11], v[212:219], v[56:59], v166, v167 op_sel_hi:[0,0,0]
	v_mfma_scale_f32_16x16x128_f8f6f4 v[52:55], v[12:19], v[212:219], v[52:55], v166, v167 op_sel_hi:[0,0,0]
	v_mfma_scale_f32_16x16x128_f8f6f4 v[48:51], v[4:11], v[220:227], v[48:51], v166, v167 op_sel_hi:[0,0,0]
	v_mfma_scale_f32_16x16x128_f8f6f4 v[44:47], v[12:19], v[220:227], v[44:47], v166, v167 op_sel_hi:[0,0,0]
	v_mfma_scale_f32_16x16x128_f8f6f4 v[40:43], v[4:11], v[228:235], v[40:43], v166, v167 op_sel_hi:[0,0,0]
	v_mfma_scale_f32_16x16x128_f8f6f4 v[36:39], v[12:19], v[228:235], v[36:39], v166, v167 op_sel_hi:[0,0,0]
	s_setprio 0
	s_barrier
	ds_read_b128 v[20:23], v186
	ds_read_b128 v[24:27], v186 offset:1024
	ds_read_b128 v[28:31], v186 offset:2048
	ds_read_b128 v[32:35], v186 offset:3072
	ds_read_b128 v[4:7], v187
	ds_read_b128 v[8:11], v187 offset:1024
	ds_read_b128 v[12:15], v187 offset:2048
	ds_read_b128 v[16:19], v187 offset:3072
	v_mov_b32_e32 v164, v176
	s_mov_b32 m0, s13
	ds_read_b128 v[204:207], v188
	ds_read_b128 v[208:211], v188 offset:1024
	ds_read_b128 v[212:215], v189
	ds_read_b128 v[216:219], v189 offset:1024
	ds_read_b128 v[220:223], v190
	ds_read_b128 v[224:227], v190 offset:1024
	ds_read_b128 v[228:231], v191
	ds_read_b128 v[232:235], v191 offset:1024
	s_nop 0
	global_load_lds_dwordx4 v164, s[2:3]
	v_mov_b32_e32 v164, v178
	s_mov_b32 m0, s12
	s_nop 0
	global_load_lds_dwordx4 v164, s[2:3]
	s_waitcnt vmcnt(8)
	s_waitcnt lgkmcnt(0)
	s_setprio 1
	s_barrier
	s_waitcnt lgkmcnt(0)
	v_mfma_scale_f32_16x16x128_f8f6f4 v[160:163], v[20:27], v[204:211], v[160:163], v166, v167 op_sel_hi:[0,0,0]
	v_mfma_scale_f32_16x16x128_f8f6f4 v[156:159], v[28:35], v[204:211], v[156:159], v166, v167 op_sel_hi:[0,0,0]
	v_mfma_scale_f32_16x16x128_f8f6f4 v[152:155], v[20:27], v[212:219], v[152:155], v166, v167 op_sel_hi:[0,0,0]
	v_mfma_scale_f32_16x16x128_f8f6f4 v[148:151], v[28:35], v[212:219], v[148:151], v166, v167 op_sel_hi:[0,0,0]
	v_mfma_scale_f32_16x16x128_f8f6f4 v[144:147], v[20:27], v[220:227], v[144:147], v166, v167 op_sel_hi:[0,0,0]
	v_mfma_scale_f32_16x16x128_f8f6f4 v[140:143], v[28:35], v[220:227], v[140:143], v166, v167 op_sel_hi:[0,0,0]
	v_mfma_scale_f32_16x16x128_f8f6f4 v[136:139], v[20:27], v[228:235], v[136:139], v166, v167 op_sel_hi:[0,0,0]
	v_mfma_scale_f32_16x16x128_f8f6f4 v[132:135], v[28:35], v[228:235], v[132:135], v166, v167 op_sel_hi:[0,0,0]
	s_setprio 0
	s_setprio 1
	v_mfma_scale_f32_16x16x128_f8f6f4 v[128:131], v[4:11], v[204:211], v[128:131], v166, v167 op_sel_hi:[0,0,0]
	v_mfma_scale_f32_16x16x128_f8f6f4 v[124:127], v[12:19], v[204:211], v[124:127], v166, v167 op_sel_hi:[0,0,0]
	v_mfma_scale_f32_16x16x128_f8f6f4 v[120:123], v[4:11], v[212:219], v[120:123], v166, v167 op_sel_hi:[0,0,0]
	v_mfma_scale_f32_16x16x128_f8f6f4 v[116:119], v[12:19], v[212:219], v[116:119], v166, v167 op_sel_hi:[0,0,0]
	v_mfma_scale_f32_16x16x128_f8f6f4 v[112:115], v[4:11], v[220:227], v[112:115], v166, v167 op_sel_hi:[0,0,0]
	v_mfma_scale_f32_16x16x128_f8f6f4 v[108:111], v[12:19], v[220:227], v[108:111], v166, v167 op_sel_hi:[0,0,0]
	v_mfma_scale_f32_16x16x128_f8f6f4 v[104:107], v[4:11], v[228:235], v[104:107], v166, v167 op_sel_hi:[0,0,0]
	v_mfma_scale_f32_16x16x128_f8f6f4 v[100:103], v[12:19], v[228:235], v[100:103], v166, v167 op_sel_hi:[0,0,0]
	s_setprio 0
	s_barrier
	s_cmp_gt_i32 s22, 1
	s_cselect_b64 s[40:41], -1, 0
	s_cmp_lt_i32 s22, 2
	s_cbranch_scc1 .LBB0_907
	s_mov_b64 s[12:13], 0
	s_cmpk_lt_u32 s21, 0x200
	s_mov_b32 s23, s21
	s_mov_b64 s[2:3], 0
	s_cbranch_scc0 .LBB0_905
	s_lshr_b32 s3, s21, 3
	s_add_i32 s23, s18, s21
	s_and_b32 s2, s21, 7
	s_sub_i32 s19, s3, 32
	s_cmpk_lt_u32 s21, 0x100
	s_cselect_b32 s3, s3, s19
	s_lshr_b32 s19, s21, 5
	s_and_b32 s19, s19, 8
	s_and_b32 s24, s3, 7
	s_or_b32 s19, s24, s19
	s_lshr_b32 s24, s3, 3
	s_lshl_b32 s3, s19, 3
	s_or_b32 s19, s3, s2
	s_mov_b64 s[2:3], -1
	s_mov_b32 s82, 0
	s_and_b64 vcc, exec, s[12:13]
	s_cbranch_vccz .LBB0_908
	s_branch .LBB0_906

.LBB0_910:
	v_mov_b32_e32 v164, v2
	v_readfirstlane_b32 s2, v168
	ds_read_b128 v[204:207], v188 offset:16384
	ds_read_b128 v[208:211], v188 offset:17408
	ds_read_b128 v[212:215], v189 offset:16384
	ds_read_b128 v[216:219], v189 offset:17408
	ds_read_b128 v[220:223], v190 offset:16384
	ds_read_b128 v[224:227], v190 offset:17408
	ds_read_b128 v[228:231], v191 offset:16384
	ds_read_b128 v[232:235], v191 offset:17408
	s_mov_b32 m0, s2
	s_add_u32 s2, s6, 0x8000
	global_load_lds_dwordx4 v164, s[6:7]
	v_mov_b32_e32 v164, v2
	v_readfirstlane_b32 s21, v169
	s_addc_u32 s3, s7, 0
	s_mov_b32 m0, s21
	v_readfirstlane_b32 s21, v170
	global_load_lds_dwordx4 v164, s[2:3]
	s_add_u32 s2, s6, 0x10000
	v_mov_b32_e32 v164, v2
	s_addc_u32 s3, s7, 0
	s_mov_b32 m0, s21
	v_readfirstlane_b32 s21, v171
	global_load_lds_dwordx4 v164, s[2:3]
	s_add_u32 s2, s6, 0x18000
	v_mov_b32_e32 v164, v2
	s_addc_u32 s3, s7, 0
	s_mov_b32 m0, s21
	s_nop 0
	global_load_lds_dwordx4 v164, s[2:3]
	v_mov_b32_e32 v164, v173
	v_readfirstlane_b32 s2, v172
	s_mov_b32 m0, s2
	v_readfirstlane_b32 s2, v174
	global_load_lds_dwordx4 v164, s[34:35]
	v_mov_b32_e32 v164, v175
	s_mov_b32 m0, s2
	s_nop 0
	global_load_lds_dwordx4 v164, s[34:35]
	s_waitcnt vmcnt(8)
	s_waitcnt lgkmcnt(0)
	s_setprio 1
	s_barrier
	s_waitcnt lgkmcnt(0)
	v_mfma_scale_f32_16x16x128_f8f6f4 v[96:99], v[20:27], v[204:211], v[96:99], v166, v167 op_sel_hi:[0,0,0]
	v_mfma_scale_f32_16x16x128_f8f6f4 v[92:95], v[28:35], v[204:211], v[92:95], v166, v167 op_sel_hi:[0,0,0]
	v_mfma_scale_f32_16x16x128_f8f6f4 v[88:91], v[20:27], v[212:219], v[88:91], v166, v167 op_sel_hi:[0,0,0]
	v_mfma_scale_f32_16x16x128_f8f6f4 v[84:87], v[28:35], v[212:219], v[84:87], v166, v167 op_sel_hi:[0,0,0]
	v_mfma_scale_f32_16x16x128_f8f6f4 v[80:83], v[20:27], v[220:227], v[80:83], v166, v167 op_sel_hi:[0,0,0]
	v_mfma_scale_f32_16x16x128_f8f6f4 v[76:79], v[28:35], v[220:227], v[76:79], v166, v167 op_sel_hi:[0,0,0]
	v_mfma_scale_f32_16x16x128_f8f6f4 v[72:75], v[20:27], v[228:235], v[72:75], v166, v167 op_sel_hi:[0,0,0]
	v_mfma_scale_f32_16x16x128_f8f6f4 v[68:71], v[28:35], v[228:235], v[68:71], v166, v167 op_sel_hi:[0,0,0]
	s_setprio 0
	s_setprio 1
	v_mfma_scale_f32_16x16x128_f8f6f4 v[64:67], v[4:11], v[204:211], v[64:67], v166, v167 op_sel_hi:[0,0,0]
	v_mfma_scale_f32_16x16x128_f8f6f4 v[60:63], v[12:19], v[204:211], v[60:63], v166, v167 op_sel_hi:[0,0,0]
	v_mfma_scale_f32_16x16x128_f8f6f4 v[56:59], v[4:11], v[212:219], v[56:59], v166, v167 op_sel_hi:[0,0,0]
	v_mfma_scale_f32_16x16x128_f8f6f4 v[52:55], v[12:19], v[212:219], v[52:55], v166, v167 op_sel_hi:[0,0,0]
	v_mfma_scale_f32_16x16x128_f8f6f4 v[48:51], v[4:11], v[220:227], v[48:51], v166, v167 op_sel_hi:[0,0,0]
	v_mfma_scale_f32_16x16x128_f8f6f4 v[44:47], v[12:19], v[220:227], v[44:47], v166, v167 op_sel_hi:[0,0,0]
	v_mfma_scale_f32_16x16x128_f8f6f4 v[40:43], v[4:11], v[228:235], v[40:43], v166, v167 op_sel_hi:[0,0,0]
	v_mfma_scale_f32_16x16x128_f8f6f4 v[36:39], v[12:19], v[228:235], v[36:39], v166, v167 op_sel_hi:[0,0,0]
	s_setprio 0
	s_barrier
	ds_read_b128 v[20:23], v201
	ds_read_b128 v[24:27], v201 offset:1024
	ds_read_b128 v[28:31], v201 offset:2048
	ds_read_b128 v[32:35], v201 offset:3072
	ds_read_b128 v[4:7], v202
	ds_read_b128 v[8:11], v202 offset:1024
	ds_read_b128 v[12:15], v202 offset:2048
	ds_read_b128 v[16:19], v202 offset:3072
	v_mov_b32_e32 v164, v176
	v_readfirstlane_b32 s2, v177
	ds_read_b128 v[204:207], v188 offset:32768
	ds_read_b128 v[208:211], v188 offset:33792
	ds_read_b128 v[212:215], v189 offset:32768
	ds_read_b128 v[216:219], v189 offset:33792
	ds_read_b128 v[220:223], v190 offset:32768
	ds_read_b128 v[224:227], v190 offset:33792
	ds_read_b128 v[228:231], v191 offset:32768
	ds_read_b128 v[232:235], v191 offset:33792
	s_mov_b32 m0, s2
	v_readfirstlane_b32 s2, v179
	global_load_lds_dwordx4 v164, s[34:35]
	v_mov_b32_e32 v164, v178
	s_mov_b32 m0, s2
	s_nop 0
	global_load_lds_dwordx4 v164, s[34:35]
	s_waitcnt vmcnt(8)
	s_waitcnt lgkmcnt(0)
	s_setprio 1
	s_barrier
	s_waitcnt lgkmcnt(0)
	v_mfma_scale_f32_16x16x128_f8f6f4 v[160:163], v[20:27], v[204:211], v[160:163], v166, v167 op_sel_hi:[0,0,0]
	v_mfma_scale_f32_16x16x128_f8f6f4 v[156:159], v[28:35], v[204:211], v[156:159], v166, v167 op_sel_hi:[0,0,0]
	v_mfma_scale_f32_16x16x128_f8f6f4 v[152:155], v[20:27], v[212:219], v[152:155], v166, v167 op_sel_hi:[0,0,0]
	v_mfma_scale_f32_16x16x128_f8f6f4 v[148:151], v[28:35], v[212:219], v[148:151], v166, v167 op_sel_hi:[0,0,0]
	v_mfma_scale_f32_16x16x128_f8f6f4 v[144:147], v[20:27], v[220:227], v[144:147], v166, v167 op_sel_hi:[0,0,0]
	v_mfma_scale_f32_16x16x128_f8f6f4 v[140:143], v[28:35], v[220:227], v[140:143], v166, v167 op_sel_hi:[0,0,0]
	v_mfma_scale_f32_16x16x128_f8f6f4 v[136:139], v[20:27], v[228:235], v[136:139], v166, v167 op_sel_hi:[0,0,0]
	v_mfma_scale_f32_16x16x128_f8f6f4 v[132:135], v[28:35], v[228:235], v[132:135], v166, v167 op_sel_hi:[0,0,0]
	s_setprio 0
	s_setprio 1
	v_mfma_scale_f32_16x16x128_f8f6f4 v[128:131], v[4:11], v[204:211], v[128:131], v166, v167 op_sel_hi:[0,0,0]
	v_mfma_scale_f32_16x16x128_f8f6f4 v[124:127], v[12:19], v[204:211], v[124:127], v166, v167 op_sel_hi:[0,0,0]
	v_mfma_scale_f32_16x16x128_f8f6f4 v[120:123], v[4:11], v[212:219], v[120:123], v166, v167 op_sel_hi:[0,0,0]
	v_mfma_scale_f32_16x16x128_f8f6f4 v[116:119], v[12:19], v[212:219], v[116:119], v166, v167 op_sel_hi:[0,0,0]
	v_mfma_scale_f32_16x16x128_f8f6f4 v[112:115], v[4:11], v[220:227], v[112:115], v166, v167 op_sel_hi:[0,0,0]
	v_mfma_scale_f32_16x16x128_f8f6f4 v[108:111], v[12:19], v[220:227], v[108:111], v166, v167 op_sel_hi:[0,0,0]
	v_mfma_scale_f32_16x16x128_f8f6f4 v[104:107], v[4:11], v[228:235], v[104:107], v166, v167 op_sel_hi:[0,0,0]
	v_mfma_scale_f32_16x16x128_f8f6f4 v[100:103], v[12:19], v[228:235], v[100:103], v166, v167 op_sel_hi:[0,0,0]
	s_setprio 0
	s_barrier
	s_add_u32 s2, s6, 0x80
	v_mov_b32_e32 v164, v2
	v_readfirstlane_b32 s21, v180
	ds_read_b128 v[204:207], v188 offset:49152
	ds_read_b128 v[208:211], v188 offset:50176
	ds_read_b128 v[212:215], v189 offset:49152
	ds_read_b128 v[216:219], v189 offset:50176
	ds_read_b128 v[220:223], v190 offset:49152
	ds_read_b128 v[224:227], v190 offset:50176
	ds_read_b128 v[228:231], v191 offset:49152
	ds_read_b128 v[232:235], v191 offset:50176
	s_addc_u32 s3, s7, 0
	s_mov_b32 m0, s21
	v_readfirstlane_b32 s21, v181
	global_load_lds_dwordx4 v164, s[2:3]
	s_add_u32 s2, s6, 0x8080
	v_mov_b32_e32 v164, v2
	s_addc_u32 s3, s7, 0
	s_mov_b32 m0, s21
	v_readfirstlane_b32 s21, v184
	global_load_lds_dwordx4 v164, s[2:3]
	s_add_u32 s2, s6, 0x10080
	v_mov_b32_e32 v164, v2
	s_addc_u32 s3, s7, 0
	s_mov_b32 m0, s21
	v_readfirstlane_b32 s21, v185
	global_load_lds_dwordx4 v164, s[2:3]
	s_add_u32 s2, s6, 0x18080
	v_mov_b32_e32 v164, v2
	s_addc_u32 s3, s7, 0
	s_mov_b32 m0, s21
	v_readfirstlane_b32 s21, v182
	global_load_lds_dwordx4 v164, s[2:3]
	s_add_u32 s2, s34, 0x80
	v_mov_b32_e32 v164, v173
	s_addc_u32 s3, s35, 0
	s_mov_b32 m0, s21
	v_readfirstlane_b32 s21, v183
	global_load_lds_dwordx4 v164, s[2:3]
	v_mov_b32_e32 v164, v175
	s_mov_b32 m0, s21
	s_nop 0
	global_load_lds_dwordx4 v164, s[2:3]
	s_waitcnt vmcnt(8)
	s_waitcnt lgkmcnt(0)
	s_setprio 1
	s_barrier
	s_waitcnt lgkmcnt(0)
	v_mfma_scale_f32_16x16x128_f8f6f4 v[96:99], v[20:27], v[204:211], v[96:99], v166, v167 op_sel_hi:[0,0,0]
	v_mfma_scale_f32_16x16x128_f8f6f4 v[92:95], v[28:35], v[204:211], v[92:95], v166, v167 op_sel_hi:[0,0,0]
	v_mfma_scale_f32_16x16x128_f8f6f4 v[88:91], v[20:27], v[212:219], v[88:91], v166, v167 op_sel_hi:[0,0,0]
	v_mfma_scale_f32_16x16x128_f8f6f4 v[84:87], v[28:35], v[212:219], v[84:87], v166, v167 op_sel_hi:[0,0,0]
	v_mfma_scale_f32_16x16x128_f8f6f4 v[80:83], v[20:27], v[220:227], v[80:83], v166, v167 op_sel_hi:[0,0,0]
	v_mfma_scale_f32_16x16x128_f8f6f4 v[76:79], v[28:35], v[220:227], v[76:79], v166, v167 op_sel_hi:[0,0,0]
	v_mfma_scale_f32_16x16x128_f8f6f4 v[72:75], v[20:27], v[228:235], v[72:75], v166, v167 op_sel_hi:[0,0,0]
	v_mfma_scale_f32_16x16x128_f8f6f4 v[68:71], v[28:35], v[228:235], v[68:71], v166, v167 op_sel_hi:[0,0,0]
	s_setprio 0
	s_setprio 1
	v_mfma_scale_f32_16x16x128_f8f6f4 v[64:67], v[4:11], v[204:211], v[64:67], v166, v167 op_sel_hi:[0,0,0]
	v_mfma_scale_f32_16x16x128_f8f6f4 v[60:63], v[12:19], v[204:211], v[60:63], v166, v167 op_sel_hi:[0,0,0]
	v_mfma_scale_f32_16x16x128_f8f6f4 v[56:59], v[4:11], v[212:219], v[56:59], v166, v167 op_sel_hi:[0,0,0]
	v_mfma_scale_f32_16x16x128_f8f6f4 v[52:55], v[12:19], v[212:219], v[52:55], v166, v167 op_sel_hi:[0,0,0]
	v_mfma_scale_f32_16x16x128_f8f6f4 v[48:51], v[4:11], v[220:227], v[48:51], v166, v167 op_sel_hi:[0,0,0]
	v_mfma_scale_f32_16x16x128_f8f6f4 v[44:47], v[12:19], v[220:227], v[44:47], v166, v167 op_sel_hi:[0,0,0]
	v_mfma_scale_f32_16x16x128_f8f6f4 v[40:43], v[4:11], v[228:235], v[40:43], v166, v167 op_sel_hi:[0,0,0]
	v_mfma_scale_f32_16x16x128_f8f6f4 v[36:39], v[12:19], v[228:235], v[36:39], v166, v167 op_sel_hi:[0,0,0]
	s_setprio 0
	s_barrier
	s_and_saveexec_b64 s[2:3], s[38:39]
	s_cbranch_execz .LBB0_912
	s_barrier

.LBB0_1008:
	s_lshl_b64 s[2:3], s[82:83], 7
	s_add_u32 s26, s10, s2
	v_mov_b32_e32 v2, v201
	v_readfirstlane_b32 s28, v204
	ds_read_b128 v[180:183], v226 offset:16384
	ds_read_b128 v[184:187], v226 offset:17408
	ds_read_b128 v[188:191], v227 offset:16384
	ds_read_b128 v[192:195], v227 offset:17408
	ds_read_b128 v[230:233], v228 offset:16384
	ds_read_b128 v[234:237], v228 offset:17408
	ds_read_b128 v[238:241], v229 offset:16384
	ds_read_b128 v[242:245], v229 offset:17408
	s_addc_u32 s27, s11, s3
	s_mov_b32 m0, s28
	s_add_u32 s28, s26, 0x10000
	global_load_lds_dwordx4 v2, s[26:27]
	v_mov_b32_e32 v2, v201
	v_readfirstlane_b32 s30, v205
	s_addc_u32 s29, s27, 0
	s_mov_b32 m0, s30
	v_readfirstlane_b32 s30, v206
	global_load_lds_dwordx4 v2, s[28:29]
	s_add_u32 s28, s26, 0x20000
	v_mov_b32_e32 v2, v201
	s_addc_u32 s29, s27, 0
	s_mov_b32 m0, s30
	s_add_u32 s26, s26, 0x30000
	global_load_lds_dwordx4 v2, s[28:29]
	v_mov_b32_e32 v2, v201
	v_readfirstlane_b32 s28, v207
	s_addc_u32 s27, s27, 0
	s_mov_b32 m0, s28
	s_add_u32 s2, s8, s2
	global_load_lds_dwordx4 v2, s[26:27]
	v_mov_b32_e32 v2, v209
	v_readfirstlane_b32 s26, v208
	s_addc_u32 s3, s9, s3
	s_mov_b32 m0, s26
	v_readfirstlane_b32 s26, v213
	global_load_lds_dwordx4 v2, s[2:3]
	v_mov_b32_e32 v2, v210
	s_mov_b32 m0, s26
	s_nop 0
	global_load_lds_dwordx4 v2, s[2:3]
	s_waitcnt vmcnt(8)
	s_waitcnt lgkmcnt(0)
	s_setprio 1
	s_barrier
	s_waitcnt lgkmcnt(0)
	v_mfma_scale_f32_16x16x128_f8f6f4 v[112:115], v[20:27], v[180:187], v[112:115], v202, v203 op_sel_hi:[0,0,0]
	v_mfma_scale_f32_16x16x128_f8f6f4 v[108:111], v[28:35], v[180:187], v[108:111], v202, v203 op_sel_hi:[0,0,0]
	v_mfma_scale_f32_16x16x128_f8f6f4 v[104:107], v[20:27], v[188:195], v[104:107], v202, v203 op_sel_hi:[0,0,0]
	v_mfma_scale_f32_16x16x128_f8f6f4 v[100:103], v[28:35], v[188:195], v[100:103], v202, v203 op_sel_hi:[0,0,0]
	v_mfma_scale_f32_16x16x128_f8f6f4 v[96:99], v[20:27], v[230:237], v[96:99], v202, v203 op_sel_hi:[0,0,0]
	v_mfma_scale_f32_16x16x128_f8f6f4 v[92:95], v[28:35], v[230:237], v[92:95], v202, v203 op_sel_hi:[0,0,0]
	v_mfma_scale_f32_16x16x128_f8f6f4 v[88:91], v[20:27], v[238:245], v[88:91], v202, v203 op_sel_hi:[0,0,0]
	v_mfma_scale_f32_16x16x128_f8f6f4 v[84:87], v[28:35], v[238:245], v[84:87], v202, v203 op_sel_hi:[0,0,0]
	s_setprio 0
	s_setprio 1
	v_mfma_scale_f32_16x16x128_f8f6f4 v[80:83], v[4:11], v[180:187], v[80:83], v202, v203 op_sel_hi:[0,0,0]
	v_mfma_scale_f32_16x16x128_f8f6f4 v[76:79], v[12:19], v[180:187], v[76:79], v202, v203 op_sel_hi:[0,0,0]
	v_mfma_scale_f32_16x16x128_f8f6f4 v[72:75], v[4:11], v[188:195], v[72:75], v202, v203 op_sel_hi:[0,0,0]
	v_mfma_scale_f32_16x16x128_f8f6f4 v[68:71], v[12:19], v[188:195], v[68:71], v202, v203 op_sel_hi:[0,0,0]
	v_mfma_scale_f32_16x16x128_f8f6f4 v[64:67], v[4:11], v[230:237], v[64:67], v202, v203 op_sel_hi:[0,0,0]
	v_mfma_scale_f32_16x16x128_f8f6f4 v[60:63], v[12:19], v[230:237], v[60:63], v202, v203 op_sel_hi:[0,0,0]
	v_mfma_scale_f32_16x16x128_f8f6f4 v[56:59], v[4:11], v[238:245], v[56:59], v202, v203 op_sel_hi:[0,0,0]
	v_mfma_scale_f32_16x16x128_f8f6f4 v[52:55], v[12:19], v[238:245], v[52:55], v202, v203 op_sel_hi:[0,0,0]
	s_setprio 0
	s_barrier
	ds_read_b128 v[20:23], v224
	ds_read_b128 v[24:27], v224 offset:1024
	ds_read_b128 v[28:31], v224 offset:2048
	ds_read_b128 v[32:35], v224 offset:3072
	ds_read_b128 v[4:7], v225
	ds_read_b128 v[8:11], v225 offset:1024
	ds_read_b128 v[12:15], v225 offset:2048
	ds_read_b128 v[16:19], v225 offset:3072
	v_mov_b32_e32 v2, v211
	v_readfirstlane_b32 s26, v214
	ds_read_b128 v[180:183], v226 offset:32768
	ds_read_b128 v[184:187], v226 offset:33792
	ds_read_b128 v[188:191], v227 offset:32768
	ds_read_b128 v[192:195], v227 offset:33792
	ds_read_b128 v[230:233], v228 offset:32768
	ds_read_b128 v[234:237], v228 offset:33792
	ds_read_b128 v[238:241], v229 offset:32768
	ds_read_b128 v[242:245], v229 offset:33792
	s_mov_b32 m0, s26
	v_readfirstlane_b32 s26, v215
	global_load_lds_dwordx4 v2, s[2:3]
	v_mov_b32_e32 v2, v212
	s_mov_b32 m0, s26
	s_nop 0
	global_load_lds_dwordx4 v2, s[2:3]
	s_waitcnt vmcnt(8)
	s_waitcnt lgkmcnt(0)
	s_setprio 1
	s_barrier
	s_waitcnt lgkmcnt(0)
	v_mfma_scale_f32_16x16x128_f8f6f4 v[176:179], v[20:27], v[180:187], v[176:179], v202, v203 op_sel_hi:[0,0,0]
	v_mfma_scale_f32_16x16x128_f8f6f4 v[172:175], v[28:35], v[180:187], v[172:175], v202, v203 op_sel_hi:[0,0,0]
	v_mfma_scale_f32_16x16x128_f8f6f4 v[168:171], v[20:27], v[188:195], v[168:171], v202, v203 op_sel_hi:[0,0,0]
	v_mfma_scale_f32_16x16x128_f8f6f4 v[164:167], v[28:35], v[188:195], v[164:167], v202, v203 op_sel_hi:[0,0,0]
	v_mfma_scale_f32_16x16x128_f8f6f4 v[160:163], v[20:27], v[230:237], v[160:163], v202, v203 op_sel_hi:[0,0,0]
	v_mfma_scale_f32_16x16x128_f8f6f4 v[156:159], v[28:35], v[230:237], v[156:159], v202, v203 op_sel_hi:[0,0,0]
	v_mfma_scale_f32_16x16x128_f8f6f4 v[152:155], v[20:27], v[238:245], v[152:155], v202, v203 op_sel_hi:[0,0,0]
	v_mfma_scale_f32_16x16x128_f8f6f4 v[148:151], v[28:35], v[238:245], v[148:151], v202, v203 op_sel_hi:[0,0,0]
	s_setprio 0
	s_setprio 1
	v_mfma_scale_f32_16x16x128_f8f6f4 v[144:147], v[4:11], v[180:187], v[144:147], v202, v203 op_sel_hi:[0,0,0]
	v_mfma_scale_f32_16x16x128_f8f6f4 v[140:143], v[12:19], v[180:187], v[140:143], v202, v203 op_sel_hi:[0,0,0]
	v_mfma_scale_f32_16x16x128_f8f6f4 v[136:139], v[4:11], v[188:195], v[136:139], v202, v203 op_sel_hi:[0,0,0]
	v_mfma_scale_f32_16x16x128_f8f6f4 v[132:135], v[12:19], v[188:195], v[132:135], v202, v203 op_sel_hi:[0,0,0]
	v_mfma_scale_f32_16x16x128_f8f6f4 v[128:131], v[4:11], v[230:237], v[128:131], v202, v203 op_sel_hi:[0,0,0]
	v_mfma_scale_f32_16x16x128_f8f6f4 v[124:127], v[12:19], v[230:237], v[124:127], v202, v203 op_sel_hi:[0,0,0]
	v_mfma_scale_f32_16x16x128_f8f6f4 v[120:123], v[4:11], v[238:245], v[120:123], v202, v203 op_sel_hi:[0,0,0]
	v_mfma_scale_f32_16x16x128_f8f6f4 v[116:119], v[12:19], v[238:245], v[116:119], v202, v203 op_sel_hi:[0,0,0]
	s_setprio 0
	s_barrier
	s_add_i32 s82, s82, 1
	s_lshl_b64 s[2:3], s[82:83], 7
	s_add_u32 s26, s10, s2
	v_mov_b32_e32 v2, v201
	v_readfirstlane_b32 s28, v216
	ds_read_b128 v[180:183], v226 offset:49152
	ds_read_b128 v[184:187], v226 offset:50176
	ds_read_b128 v[188:191], v227 offset:49152
	ds_read_b128 v[192:195], v227 offset:50176
	ds_read_b128 v[230:233], v228 offset:49152
	ds_read_b128 v[234:237], v228 offset:50176
	ds_read_b128 v[238:241], v229 offset:49152
	ds_read_b128 v[242:245], v229 offset:50176
	s_addc_u32 s27, s11, s3
	s_mov_b32 m0, s28
	s_add_u32 s28, s26, 0x10000
	global_load_lds_dwordx4 v2, s[26:27]
	v_mov_b32_e32 v2, v201
	v_readfirstlane_b32 s30, v217
	s_addc_u32 s29, s27, 0
	s_mov_b32 m0, s30
	v_readfirstlane_b32 s30, v220
	global_load_lds_dwordx4 v2, s[28:29]
	s_add_u32 s28, s26, 0x20000
	v_mov_b32_e32 v2, v201
	s_addc_u32 s29, s27, 0
	s_mov_b32 m0, s30
	s_add_u32 s26, s26, 0x30000
	global_load_lds_dwordx4 v2, s[28:29]
	v_mov_b32_e32 v2, v201
	v_readfirstlane_b32 s28, v221
	s_addc_u32 s27, s27, 0
	s_mov_b32 m0, s28
	s_add_u32 s2, s8, s2
	global_load_lds_dwordx4 v2, s[26:27]
	v_mov_b32_e32 v2, v209
	v_readfirstlane_b32 s26, v218
	s_addc_u32 s3, s9, s3
	s_mov_b32 m0, s26
	v_readfirstlane_b32 s26, v219
	global_load_lds_dwordx4 v2, s[2:3]
	v_mov_b32_e32 v2, v210
	s_mov_b32 m0, s26
	s_nop 0
	global_load_lds_dwordx4 v2, s[2:3]
	s_waitcnt vmcnt(8)
	s_waitcnt lgkmcnt(0)
	s_setprio 1
	s_barrier
	s_waitcnt lgkmcnt(0)
	v_mfma_scale_f32_16x16x128_f8f6f4 v[112:115], v[20:27], v[180:187], v[112:115], v202, v203 op_sel_hi:[0,0,0]
	v_mfma_scale_f32_16x16x128_f8f6f4 v[108:111], v[28:35], v[180:187], v[108:111], v202, v203 op_sel_hi:[0,0,0]
	v_mfma_scale_f32_16x16x128_f8f6f4 v[104:107], v[20:27], v[188:195], v[104:107], v202, v203 op_sel_hi:[0,0,0]
	v_mfma_scale_f32_16x16x128_f8f6f4 v[100:103], v[28:35], v[188:195], v[100:103], v202, v203 op_sel_hi:[0,0,0]
	v_mfma_scale_f32_16x16x128_f8f6f4 v[96:99], v[20:27], v[230:237], v[96:99], v202, v203 op_sel_hi:[0,0,0]
	v_mfma_scale_f32_16x16x128_f8f6f4 v[92:95], v[28:35], v[230:237], v[92:95], v202, v203 op_sel_hi:[0,0,0]
	v_mfma_scale_f32_16x16x128_f8f6f4 v[88:91], v[20:27], v[238:245], v[88:91], v202, v203 op_sel_hi:[0,0,0]
	v_mfma_scale_f32_16x16x128_f8f6f4 v[84:87], v[28:35], v[238:245], v[84:87], v202, v203 op_sel_hi:[0,0,0]
	s_setprio 0
	s_setprio 1
	v_mfma_scale_f32_16x16x128_f8f6f4 v[80:83], v[4:11], v[180:187], v[80:83], v202, v203 op_sel_hi:[0,0,0]
	v_mfma_scale_f32_16x16x128_f8f6f4 v[76:79], v[12:19], v[180:187], v[76:79], v202, v203 op_sel_hi:[0,0,0]
	v_mfma_scale_f32_16x16x128_f8f6f4 v[72:75], v[4:11], v[188:195], v[72:75], v202, v203 op_sel_hi:[0,0,0]
	v_mfma_scale_f32_16x16x128_f8f6f4 v[68:71], v[12:19], v[188:195], v[68:71], v202, v203 op_sel_hi:[0,0,0]
	v_mfma_scale_f32_16x16x128_f8f6f4 v[64:67], v[4:11], v[230:237], v[64:67], v202, v203 op_sel_hi:[0,0,0]
	v_mfma_scale_f32_16x16x128_f8f6f4 v[60:63], v[12:19], v[230:237], v[60:63], v202, v203 op_sel_hi:[0,0,0]
	v_mfma_scale_f32_16x16x128_f8f6f4 v[56:59], v[4:11], v[238:245], v[56:59], v202, v203 op_sel_hi:[0,0,0]
	v_mfma_scale_f32_16x16x128_f8f6f4 v[52:55], v[12:19], v[238:245], v[52:55], v202, v203 op_sel_hi:[0,0,0]
	s_setprio 0
	s_barrier
	s_add_i32 s25, s25, 2
	s_add_u32 s40, s40, 0x100
	s_addc_u32 s41, s41, 0
	s_cmp_gt_u32 s25, 5
	s_cbranch_scc1 .LBB0_1015

.LBB0_1011:
	ds_read_b128 v[20:23], v222
	ds_read_b128 v[24:27], v222 offset:1024
	ds_read_b128 v[28:31], v222 offset:2048
	ds_read_b128 v[32:35], v222 offset:3072
	ds_read_b128 v[4:7], v223
	ds_read_b128 v[8:11], v223 offset:1024
	ds_read_b128 v[12:15], v223 offset:2048
	ds_read_b128 v[16:19], v223 offset:3072
	v_add_u32_e32 v246, 0xc000, v208
	s_add_u32 s26, s40, 0x80
	v_mov_b32_e32 v2, v211
	v_readfirstlane_b32 s28, v246
	v_add_u32_e32 v246, 0xe000, v208
	ds_read_b128 v[180:183], v226
	ds_read_b128 v[184:187], v226 offset:1024
	ds_read_b128 v[230:233], v227
	ds_read_b128 v[234:237], v227 offset:1024
	ds_read_b128 v[238:241], v228
	ds_read_b128 v[242:245], v228 offset:1024
	ds_read_b128 v[188:191], v229
	ds_read_b128 v[192:195], v229 offset:1024
	s_addc_u32 s27, s41, 0
	s_mov_b32 m0, s28
	v_readfirstlane_b32 s28, v246
	global_load_lds_dwordx4 v2, s[26:27]
	v_mov_b32_e32 v2, v212
	s_mov_b32 m0, s28
	s_nop 0
	global_load_lds_dwordx4 v2, s[26:27]
	s_waitcnt vmcnt(8)
	s_waitcnt lgkmcnt(0)
	s_setprio 1
	s_barrier
	s_waitcnt lgkmcnt(0)
	v_mfma_scale_f32_16x16x128_f8f6f4 v[176:179], v[20:27], v[180:187], v[176:179], v202, v203 op_sel_hi:[0,0,0]
	v_mfma_scale_f32_16x16x128_f8f6f4 v[172:175], v[28:35], v[180:187], v[172:175], v202, v203 op_sel_hi:[0,0,0]
	v_mfma_scale_f32_16x16x128_f8f6f4 v[168:171], v[20:27], v[230:237], v[168:171], v202, v203 op_sel_hi:[0,0,0]
	v_mfma_scale_f32_16x16x128_f8f6f4 v[164:167], v[28:35], v[230:237], v[164:167], v202, v203 op_sel_hi:[0,0,0]
	v_mfma_scale_f32_16x16x128_f8f6f4 v[160:163], v[20:27], v[238:245], v[160:163], v202, v203 op_sel_hi:[0,0,0]
	v_mfma_scale_f32_16x16x128_f8f6f4 v[156:159], v[28:35], v[238:245], v[156:159], v202, v203 op_sel_hi:[0,0,0]
	v_mfma_scale_f32_16x16x128_f8f6f4 v[152:155], v[20:27], v[188:195], v[152:155], v202, v203 op_sel_hi:[0,0,0]
	v_mfma_scale_f32_16x16x128_f8f6f4 v[148:151], v[28:35], v[188:195], v[148:151], v202, v203 op_sel_hi:[0,0,0]
	s_setprio 0
	s_setprio 1
	v_mfma_scale_f32_16x16x128_f8f6f4 v[144:147], v[4:11], v[180:187], v[144:147], v202, v203 op_sel_hi:[0,0,0]
	v_mfma_scale_f32_16x16x128_f8f6f4 v[140:143], v[12:19], v[180:187], v[140:143], v202, v203 op_sel_hi:[0,0,0]
	v_mfma_scale_f32_16x16x128_f8f6f4 v[136:139], v[4:11], v[230:237], v[136:139], v202, v203 op_sel_hi:[0,0,0]
	v_mfma_scale_f32_16x16x128_f8f6f4 v[132:135], v[12:19], v[230:237], v[132:135], v202, v203 op_sel_hi:[0,0,0]
	v_mfma_scale_f32_16x16x128_f8f6f4 v[128:131], v[4:11], v[238:245], v[128:131], v202, v203 op_sel_hi:[0,0,0]
	v_mfma_scale_f32_16x16x128_f8f6f4 v[124:127], v[12:19], v[238:245], v[124:127], v202, v203 op_sel_hi:[0,0,0]
	v_mfma_scale_f32_16x16x128_f8f6f4 v[120:123], v[4:11], v[188:195], v[120:123], v202, v203 op_sel_hi:[0,0,0]
	v_mfma_scale_f32_16x16x128_f8f6f4 v[116:119], v[12:19], v[188:195], v[116:119], v202, v203 op_sel_hi:[0,0,0]
	s_setprio 0
	s_barrier
	s_andn2_b64 vcc, exec, s[2:3]
	s_cbranch_vccnz .LBB0_1014
	s_cmpk_gt_u32 s19, 0x1ff
	s_mov_b64 s[20:21], 0
	s_cbranch_scc1 .LBB0_1007
	v_mov_b32_e32 v2, v0
	s_lshr_b32 s3, s19, 3
	v_ashrrev_i32_e32 v181, 31, v2
	v_lshrrev_b32_e32 v181, 26, v181
	v_lshlrev_b32_e32 v180, 4, v2
	v_add_u32_e32 v181, v2, v181
	v_bfe_i32 v2, v2, 27, 1
	v_lshrrev_b32_e32 v2, 22, v2
	v_add_u32_e32 v2, v180, v2
	v_and_b32_e32 v2, 0xfffffc00, v2
	v_sub_u32_e32 v2, v180, v2
	v_lshrrev_b32_e32 v180, 4, v2
	s_add_i32 s6, s18, s19
	s_and_b32 s2, s19, 7
	s_sub_i32 s10, s3, 32
	v_bitop3_b32 v2, v180, v2, 32 bitop3:0x6c
	s_cmpk_lt_u32 s19, 0x100
	v_ashrrev_i32_e32 v182, 31, v2
	s_cselect_b32 s3, s3, s10
	s_lshr_b32 s10, s19, 5
	v_lshrrev_b32_e32 v182, 26, v182
	s_and_b32 s10, s10, 8
	s_and_b32 s11, s3, 7
	v_add_u32_e32 v182, v2, v182
	s_or_b32 s10, s11, s10
	v_lshrrev_b32_e32 v183, 6, v182
	v_and_b32_e32 v182, 0xc0, v182
	s_lshr_b32 s82, s3, 3
	s_lshl_b32 s3, s10, 3
	v_ashrrev_i32_e32 v181, 6, v181
	v_sub_u32_e32 v2, v2, v182
	s_or_b32 s16, s3, s2
	v_lshlrev_b32_e32 v180, 3, v181
	v_lshlrev_b32_e32 v181, 5, v181
	v_ashrrev_i16_sdwa v2, v196, sext(v2) dst_sel:DWORD dst_unused:UNUSED_PAD src0_sel:DWORD src1_sel:BYTE_0
	s_lshl_b64 s[2:3], s[82:83], 18
	v_and_b32_e32 v180, 0x3ffff0, v180
	v_and_b32_e32 v181, 32, v181
	v_bfe_i32 v2, v2, 0, 16
	s_add_u32 s10, s7, s2
	s_addc_u32 s11, s17, s3
	s_lshl_b32 s2, s16, 18
	v_add_lshl_u32 v180, v183, v180, 10
	v_add_lshl_u32 v2, v181, v2, 1
	v_add3_u32 v209, v180, s2, v2
	v_add_u32_e32 v210, 0x10000, v209
	v_add_u32_e32 v211, 0x20000, v209
	v_add_u32_e32 v212, 0x30000, v209
	s_mov_b64 s[20:21], -1
	s_mov_b32 s19, s6
	s_mov_b32 s6, s82
	s_branch .LBB0_1007

.LBB0_1248:
	ds_read_b128 v[20:23], v212
	ds_read_b128 v[24:27], v212 offset:1024
	ds_read_b128 v[28:31], v212 offset:2048
	ds_read_b128 v[32:35], v212 offset:3072
	ds_read_b128 v[4:7], v213
	ds_read_b128 v[8:11], v213 offset:1024
	ds_read_b128 v[12:15], v213 offset:2048
	ds_read_b128 v[16:19], v213 offset:3072
	s_lshl_b32 s2, s30, 7
	s_add_u32 s2, s6, s2
	s_addc_u32 s3, s7, 0
	v_add_u32_e32 v181, 0xc000, v202
	s_add_u32 s2, s2, 0x80
	v_mov_b32_e32 v2, v185
	v_readfirstlane_b32 s31, v181
	v_add_u32_e32 v181, 0xe000, v202
	ds_read_b128 v[220:223], v216
	ds_read_b128 v[224:227], v216 offset:1024
	ds_read_b128 v[228:231], v217
	ds_read_b128 v[232:235], v217 offset:1024
	ds_read_b128 v[236:239], v218
	ds_read_b128 v[240:243], v218 offset:1024
	ds_read_b128 v[244:247], v219
	ds_read_b128 v[248:251], v219 offset:1024
	s_addc_u32 s3, s3, 0
	s_mov_b32 m0, s31
	v_readfirstlane_b32 s31, v181
	global_load_lds_dwordx4 v2, s[2:3]
	v_mov_b32_e32 v2, v186
	s_mov_b32 m0, s31
	s_nop 0
	global_load_lds_dwordx4 v2, s[2:3]
	s_waitcnt vmcnt(8)
	s_waitcnt lgkmcnt(0)
	s_setprio 1
	s_barrier
	s_waitcnt lgkmcnt(0)
	v_mfma_scale_f32_16x16x128_f8f6f4 v[176:179], v[20:27], v[220:227], v[176:179], v188, v187 op_sel_hi:[0,0,0]
	v_mfma_scale_f32_16x16x128_f8f6f4 v[168:171], v[28:35], v[220:227], v[168:171], v188, v187 op_sel_hi:[0,0,0]
	v_mfma_scale_f32_16x16x128_f8f6f4 v[160:163], v[20:27], v[228:235], v[160:163], v188, v187 op_sel_hi:[0,0,0]
	v_mfma_scale_f32_16x16x128_f8f6f4 v[152:155], v[28:35], v[228:235], v[152:155], v188, v187 op_sel_hi:[0,0,0]
	v_mfma_scale_f32_16x16x128_f8f6f4 v[144:147], v[20:27], v[236:243], v[144:147], v188, v187 op_sel_hi:[0,0,0]
	v_mfma_scale_f32_16x16x128_f8f6f4 v[136:139], v[28:35], v[236:243], v[136:139], v188, v187 op_sel_hi:[0,0,0]
	v_mfma_scale_f32_16x16x128_f8f6f4 v[128:131], v[20:27], v[244:251], v[128:131], v188, v187 op_sel_hi:[0,0,0]
	v_mfma_scale_f32_16x16x128_f8f6f4 v[120:123], v[28:35], v[244:251], v[120:123], v188, v187 op_sel_hi:[0,0,0]
	s_setprio 0
	s_setprio 1
	s_add_i32 s31, s30, 2
	v_mfma_scale_f32_16x16x128_f8f6f4 v[172:175], v[4:11], v[220:227], v[172:175], v188, v187 op_sel_hi:[0,0,0]
	v_mfma_scale_f32_16x16x128_f8f6f4 v[164:167], v[12:19], v[220:227], v[164:167], v188, v187 op_sel_hi:[0,0,0]
	v_mfma_scale_f32_16x16x128_f8f6f4 v[156:159], v[4:11], v[228:235], v[156:159], v188, v187 op_sel_hi:[0,0,0]
	v_mfma_scale_f32_16x16x128_f8f6f4 v[148:151], v[12:19], v[228:235], v[148:151], v188, v187 op_sel_hi:[0,0,0]
	v_mfma_scale_f32_16x16x128_f8f6f4 v[140:143], v[4:11], v[236:243], v[140:143], v188, v187 op_sel_hi:[0,0,0]
	v_mfma_scale_f32_16x16x128_f8f6f4 v[132:135], v[12:19], v[236:243], v[132:135], v188, v187 op_sel_hi:[0,0,0]
	v_mfma_scale_f32_16x16x128_f8f6f4 v[124:127], v[4:11], v[244:251], v[124:127], v188, v187 op_sel_hi:[0,0,0]
	v_mfma_scale_f32_16x16x128_f8f6f4 v[116:119], v[12:19], v[244:251], v[116:119], v188, v187 op_sel_hi:[0,0,0]
	s_cmp_lg_u32 s30, 6
	s_setprio 0
	s_barrier
	s_cbranch_scc1 .LBB0_1253
	s_mov_b64 s[2:3], -1
	s_cmp_ge_u32 s18, s16
	s_mov_b64 s[12:13], -1
	s_cbranch_scc1 .LBB0_1251

.LBB0_1259:
	s_lshl_b64 s[2:3], s[82:83], 7
	s_add_u32 s34, s4, s2
	v_mov_b32_e32 v2, v184
	v_readfirstlane_b32 s33, v189
	ds_read_b128 v[220:223], v216 offset:16384
	ds_read_b128 v[224:227], v216 offset:17408
	ds_read_b128 v[228:231], v217 offset:16384
	ds_read_b128 v[232:235], v217 offset:17408
	ds_read_b128 v[236:239], v218 offset:16384
	ds_read_b128 v[240:243], v218 offset:17408
	ds_read_b128 v[244:247], v219 offset:16384
	ds_read_b128 v[248:251], v219 offset:17408
	s_addc_u32 s35, s5, s3
	s_mov_b32 m0, s33
	s_add_u32 s40, s34, 0x10000
	global_load_lds_dwordx4 v2, s[34:35]
	v_mov_b32_e32 v2, v184
	v_readfirstlane_b32 s33, v190
	s_addc_u32 s41, s35, 0
	s_mov_b32 m0, s33
	v_readfirstlane_b32 s33, v191
	global_load_lds_dwordx4 v2, s[40:41]
	s_add_u32 s40, s34, 0x20000
	v_mov_b32_e32 v2, v184
	s_addc_u32 s41, s35, 0
	s_mov_b32 m0, s33
	s_add_u32 s34, s34, 0x30000
	global_load_lds_dwordx4 v2, s[40:41]
	v_mov_b32_e32 v2, v184
	v_readfirstlane_b32 s33, v201
	s_addc_u32 s35, s35, 0
	s_mov_b32 m0, s33
	s_add_u32 s2, s6, s2
	global_load_lds_dwordx4 v2, s[34:35]
	v_mov_b32_e32 v2, v182
	v_readfirstlane_b32 s33, v202
	s_addc_u32 s3, s7, s3
	s_mov_b32 m0, s33
	v_readfirstlane_b32 s33, v203
	global_load_lds_dwordx4 v2, s[2:3]
	v_mov_b32_e32 v2, v183
	s_mov_b32 m0, s33
	s_nop 0
	global_load_lds_dwordx4 v2, s[2:3]
	s_waitcnt vmcnt(8)
	s_waitcnt lgkmcnt(0)
	s_setprio 1
	s_barrier
	s_waitcnt lgkmcnt(0)
	v_mfma_scale_f32_16x16x128_f8f6f4 v[112:115], v[20:27], v[220:227], v[112:115], v188, v187 op_sel_hi:[0,0,0]
	v_mfma_scale_f32_16x16x128_f8f6f4 v[104:107], v[28:35], v[220:227], v[104:107], v188, v187 op_sel_hi:[0,0,0]
	v_mfma_scale_f32_16x16x128_f8f6f4 v[96:99], v[20:27], v[228:235], v[96:99], v188, v187 op_sel_hi:[0,0,0]
	v_mfma_scale_f32_16x16x128_f8f6f4 v[88:91], v[28:35], v[228:235], v[88:91], v188, v187 op_sel_hi:[0,0,0]
	v_mfma_scale_f32_16x16x128_f8f6f4 v[80:83], v[20:27], v[236:243], v[80:83], v188, v187 op_sel_hi:[0,0,0]
	v_mfma_scale_f32_16x16x128_f8f6f4 v[72:75], v[28:35], v[236:243], v[72:75], v188, v187 op_sel_hi:[0,0,0]
	v_mfma_scale_f32_16x16x128_f8f6f4 v[64:67], v[20:27], v[244:251], v[64:67], v188, v187 op_sel_hi:[0,0,0]
	v_mfma_scale_f32_16x16x128_f8f6f4 v[56:59], v[28:35], v[244:251], v[56:59], v188, v187 op_sel_hi:[0,0,0]
	s_setprio 0
	s_setprio 1
	v_mfma_scale_f32_16x16x128_f8f6f4 v[108:111], v[4:11], v[220:227], v[108:111], v188, v187 op_sel_hi:[0,0,0]
	v_mfma_scale_f32_16x16x128_f8f6f4 v[100:103], v[12:19], v[220:227], v[100:103], v188, v187 op_sel_hi:[0,0,0]
	v_mfma_scale_f32_16x16x128_f8f6f4 v[92:95], v[4:11], v[228:235], v[92:95], v188, v187 op_sel_hi:[0,0,0]
	v_mfma_scale_f32_16x16x128_f8f6f4 v[84:87], v[12:19], v[228:235], v[84:87], v188, v187 op_sel_hi:[0,0,0]
	v_mfma_scale_f32_16x16x128_f8f6f4 v[76:79], v[4:11], v[236:243], v[76:79], v188, v187 op_sel_hi:[0,0,0]
	v_mfma_scale_f32_16x16x128_f8f6f4 v[68:71], v[12:19], v[236:243], v[68:71], v188, v187 op_sel_hi:[0,0,0]
	v_mfma_scale_f32_16x16x128_f8f6f4 v[60:63], v[4:11], v[244:251], v[60:63], v188, v187 op_sel_hi:[0,0,0]
	v_mfma_scale_f32_16x16x128_f8f6f4 v[52:55], v[12:19], v[244:251], v[52:55], v188, v187 op_sel_hi:[0,0,0]
	s_setprio 0
	s_barrier
	ds_read_b128 v[20:23], v214
	ds_read_b128 v[24:27], v214 offset:1024
	ds_read_b128 v[28:31], v214 offset:2048
	ds_read_b128 v[32:35], v214 offset:3072
	ds_read_b128 v[4:7], v215
	ds_read_b128 v[8:11], v215 offset:1024
	ds_read_b128 v[12:15], v215 offset:2048
	ds_read_b128 v[16:19], v215 offset:3072
	v_mov_b32_e32 v2, v185
	v_readfirstlane_b32 s33, v204
	ds_read_b128 v[220:223], v216 offset:32768
	ds_read_b128 v[224:227], v216 offset:33792
	ds_read_b128 v[228:231], v217 offset:32768
	ds_read_b128 v[232:235], v217 offset:33792
	ds_read_b128 v[236:239], v218 offset:32768
	ds_read_b128 v[240:243], v218 offset:33792
	ds_read_b128 v[244:247], v219 offset:32768
	ds_read_b128 v[248:251], v219 offset:33792
	s_mov_b32 m0, s33
	v_readfirstlane_b32 s33, v205
	global_load_lds_dwordx4 v2, s[2:3]
	v_mov_b32_e32 v2, v186
	s_mov_b32 m0, s33
	s_nop 0
	global_load_lds_dwordx4 v2, s[2:3]
	s_waitcnt vmcnt(8)
	s_waitcnt lgkmcnt(0)
	s_setprio 1
	s_barrier
	s_waitcnt lgkmcnt(0)
	v_mfma_scale_f32_16x16x128_f8f6f4 v[176:179], v[20:27], v[220:227], v[176:179], v188, v187 op_sel_hi:[0,0,0]
	v_mfma_scale_f32_16x16x128_f8f6f4 v[168:171], v[28:35], v[220:227], v[168:171], v188, v187 op_sel_hi:[0,0,0]
	v_mfma_scale_f32_16x16x128_f8f6f4 v[160:163], v[20:27], v[228:235], v[160:163], v188, v187 op_sel_hi:[0,0,0]
	v_mfma_scale_f32_16x16x128_f8f6f4 v[152:155], v[28:35], v[228:235], v[152:155], v188, v187 op_sel_hi:[0,0,0]
	v_mfma_scale_f32_16x16x128_f8f6f4 v[144:147], v[20:27], v[236:243], v[144:147], v188, v187 op_sel_hi:[0,0,0]
	v_mfma_scale_f32_16x16x128_f8f6f4 v[136:139], v[28:35], v[236:243], v[136:139], v188, v187 op_sel_hi:[0,0,0]
	v_mfma_scale_f32_16x16x128_f8f6f4 v[128:131], v[20:27], v[244:251], v[128:131], v188, v187 op_sel_hi:[0,0,0]
	v_mfma_scale_f32_16x16x128_f8f6f4 v[120:123], v[28:35], v[244:251], v[120:123], v188, v187 op_sel_hi:[0,0,0]
	s_setprio 0
	s_setprio 1
	v_mfma_scale_f32_16x16x128_f8f6f4 v[172:175], v[4:11], v[220:227], v[172:175], v188, v187 op_sel_hi:[0,0,0]
	v_mfma_scale_f32_16x16x128_f8f6f4 v[164:167], v[12:19], v[220:227], v[164:167], v188, v187 op_sel_hi:[0,0,0]
	v_mfma_scale_f32_16x16x128_f8f6f4 v[156:159], v[4:11], v[228:235], v[156:159], v188, v187 op_sel_hi:[0,0,0]
	v_mfma_scale_f32_16x16x128_f8f6f4 v[148:151], v[12:19], v[228:235], v[148:151], v188, v187 op_sel_hi:[0,0,0]
	v_mfma_scale_f32_16x16x128_f8f6f4 v[140:143], v[4:11], v[236:243], v[140:143], v188, v187 op_sel_hi:[0,0,0]
	v_mfma_scale_f32_16x16x128_f8f6f4 v[132:135], v[12:19], v[236:243], v[132:135], v188, v187 op_sel_hi:[0,0,0]
	v_mfma_scale_f32_16x16x128_f8f6f4 v[124:127], v[4:11], v[244:251], v[124:127], v188, v187 op_sel_hi:[0,0,0]
	v_mfma_scale_f32_16x16x128_f8f6f4 v[116:119], v[12:19], v[244:251], v[116:119], v188, v187 op_sel_hi:[0,0,0]
	s_setprio 0
	s_barrier
	s_add_i32 s82, s82, 1
	s_lshl_b64 s[2:3], s[82:83], 7
	s_add_u32 s34, s4, s2
	v_mov_b32_e32 v2, v184
	v_readfirstlane_b32 s33, v206
	ds_read_b128 v[220:223], v216 offset:49152
	ds_read_b128 v[224:227], v216 offset:50176
	ds_read_b128 v[228:231], v217 offset:49152
	ds_read_b128 v[232:235], v217 offset:50176
	ds_read_b128 v[236:239], v218 offset:49152
	ds_read_b128 v[240:243], v218 offset:50176
	ds_read_b128 v[244:247], v219 offset:49152
	ds_read_b128 v[248:251], v219 offset:50176
	s_addc_u32 s35, s5, s3
	s_mov_b32 m0, s33
	s_add_u32 s40, s34, 0x10000
	global_load_lds_dwordx4 v2, s[34:35]
	v_mov_b32_e32 v2, v184
	v_readfirstlane_b32 s33, v207
	s_addc_u32 s41, s35, 0
	s_mov_b32 m0, s33
	v_readfirstlane_b32 s33, v210
	global_load_lds_dwordx4 v2, s[40:41]
	s_add_u32 s40, s34, 0x20000
	v_mov_b32_e32 v2, v184
	s_addc_u32 s41, s35, 0
	s_mov_b32 m0, s33
	s_add_u32 s34, s34, 0x30000
	global_load_lds_dwordx4 v2, s[40:41]
	v_mov_b32_e32 v2, v184
	v_readfirstlane_b32 s33, v211
	s_addc_u32 s35, s35, 0
	s_mov_b32 m0, s33
	s_add_u32 s2, s6, s2
	global_load_lds_dwordx4 v2, s[34:35]
	v_mov_b32_e32 v2, v182
	v_readfirstlane_b32 s33, v208
	s_addc_u32 s3, s7, s3
	s_mov_b32 m0, s33
	v_readfirstlane_b32 s33, v209
	global_load_lds_dwordx4 v2, s[2:3]
	v_mov_b32_e32 v2, v183
	s_mov_b32 m0, s33
	s_nop 0
	global_load_lds_dwordx4 v2, s[2:3]
	s_waitcnt vmcnt(8)
	s_waitcnt lgkmcnt(0)
	s_setprio 1
	s_barrier
	s_waitcnt lgkmcnt(0)
	v_mfma_scale_f32_16x16x128_f8f6f4 v[112:115], v[20:27], v[220:227], v[112:115], v188, v187 op_sel_hi:[0,0,0]
	v_mfma_scale_f32_16x16x128_f8f6f4 v[104:107], v[28:35], v[220:227], v[104:107], v188, v187 op_sel_hi:[0,0,0]
	v_mfma_scale_f32_16x16x128_f8f6f4 v[96:99], v[20:27], v[228:235], v[96:99], v188, v187 op_sel_hi:[0,0,0]
	v_mfma_scale_f32_16x16x128_f8f6f4 v[88:91], v[28:35], v[228:235], v[88:91], v188, v187 op_sel_hi:[0,0,0]
	v_mfma_scale_f32_16x16x128_f8f6f4 v[80:83], v[20:27], v[236:243], v[80:83], v188, v187 op_sel_hi:[0,0,0]
	v_mfma_scale_f32_16x16x128_f8f6f4 v[72:75], v[28:35], v[236:243], v[72:75], v188, v187 op_sel_hi:[0,0,0]
	v_mfma_scale_f32_16x16x128_f8f6f4 v[64:67], v[20:27], v[244:251], v[64:67], v188, v187 op_sel_hi:[0,0,0]
	v_mfma_scale_f32_16x16x128_f8f6f4 v[56:59], v[28:35], v[244:251], v[56:59], v188, v187 op_sel_hi:[0,0,0]
	s_setprio 0
	s_setprio 1
	v_mfma_scale_f32_16x16x128_f8f6f4 v[108:111], v[4:11], v[220:227], v[108:111], v188, v187 op_sel_hi:[0,0,0]
	v_mfma_scale_f32_16x16x128_f8f6f4 v[100:103], v[12:19], v[220:227], v[100:103], v188, v187 op_sel_hi:[0,0,0]
	v_mfma_scale_f32_16x16x128_f8f6f4 v[92:95], v[4:11], v[228:235], v[92:95], v188, v187 op_sel_hi:[0,0,0]
	v_mfma_scale_f32_16x16x128_f8f6f4 v[84:87], v[12:19], v[228:235], v[84:87], v188, v187 op_sel_hi:[0,0,0]
	v_mfma_scale_f32_16x16x128_f8f6f4 v[76:79], v[4:11], v[236:243], v[76:79], v188, v187 op_sel_hi:[0,0,0]
	v_mfma_scale_f32_16x16x128_f8f6f4 v[68:71], v[12:19], v[236:243], v[68:71], v188, v187 op_sel_hi:[0,0,0]
	v_mfma_scale_f32_16x16x128_f8f6f4 v[60:63], v[4:11], v[244:251], v[60:63], v188, v187 op_sel_hi:[0,0,0]
	v_mfma_scale_f32_16x16x128_f8f6f4 v[52:55], v[12:19], v[244:251], v[52:55], v188, v187 op_sel_hi:[0,0,0]
	s_setprio 0
	s_barrier
	s_cmp_gt_u32 s30, 5
	s_cbranch_scc1 .LBB0_1261
	s_mov_b32 s30, s31
	s_branch .LBB0_1248

.LBB0_1387:
	ds_read_b128 v[20:23], v212
	ds_read_b128 v[24:27], v212 offset:1024
	ds_read_b128 v[28:31], v212 offset:2048
	ds_read_b128 v[32:35], v212 offset:3072
	ds_read_b128 v[4:7], v213
	ds_read_b128 v[8:11], v213 offset:1024
	ds_read_b128 v[12:15], v213 offset:2048
	ds_read_b128 v[16:19], v213 offset:3072
	s_lshl_b32 s2, s23, 7
	s_add_u32 s2, s4, s2
	s_addc_u32 s3, s5, 0
	v_add_u32_e32 v181, 0xc000, v202
	s_add_u32 s2, s2, 0x80
	v_mov_b32_e32 v2, v184
	v_readfirstlane_b32 s24, v181
	v_add_u32_e32 v181, 0xe000, v202
	ds_read_b128 v[222:225], v216
	ds_read_b128 v[226:229], v216 offset:1024
	ds_read_b128 v[230:233], v217
	ds_read_b128 v[234:237], v217 offset:1024
	ds_read_b128 v[238:241], v218
	ds_read_b128 v[242:245], v218 offset:1024
	ds_read_b128 v[36:39], v219
	ds_read_b128 v[40:43], v219 offset:1024
	s_addc_u32 s3, s3, 0
	s_mov_b32 m0, s24
	v_readfirstlane_b32 s24, v181
	global_load_lds_dwordx4 v2, s[2:3]
	v_mov_b32_e32 v2, v185
	s_mov_b32 m0, s24
	s_nop 0
	global_load_lds_dwordx4 v2, s[2:3]
	s_waitcnt vmcnt(8)
	s_waitcnt lgkmcnt(0)
	s_setprio 1
	s_barrier
	s_waitcnt lgkmcnt(0)
	v_mfma_scale_f32_16x16x128_f8f6f4 v[176:179], v[20:27], v[222:229], v[176:179], v188, v187 op_sel_hi:[0,0,0]
	v_mfma_scale_f32_16x16x128_f8f6f4 v[172:175], v[28:35], v[222:229], v[172:175], v188, v187 op_sel_hi:[0,0,0]
	v_mfma_scale_f32_16x16x128_f8f6f4 v[168:171], v[20:27], v[230:237], v[168:171], v188, v187 op_sel_hi:[0,0,0]
	v_mfma_scale_f32_16x16x128_f8f6f4 v[164:167], v[28:35], v[230:237], v[164:167], v188, v187 op_sel_hi:[0,0,0]
	v_mfma_scale_f32_16x16x128_f8f6f4 v[160:163], v[20:27], v[238:245], v[160:163], v188, v187 op_sel_hi:[0,0,0]
	v_mfma_scale_f32_16x16x128_f8f6f4 v[156:159], v[28:35], v[238:245], v[156:159], v188, v187 op_sel_hi:[0,0,0]
	v_mfma_scale_f32_16x16x128_f8f6f4 v[152:155], v[20:27], v[36:43], v[152:155], v188, v187 op_sel_hi:[0,0,0]
	v_mfma_scale_f32_16x16x128_f8f6f4 v[148:151], v[28:35], v[36:43], v[148:151], v188, v187 op_sel_hi:[0,0,0]
	s_setprio 0
	s_setprio 1
	s_add_i32 s24, s23, 2
	v_mfma_scale_f32_16x16x128_f8f6f4 v[120:123], v[4:11], v[222:229], v[120:123], v188, v187 op_sel_hi:[0,0,0]
	v_mfma_scale_f32_16x16x128_f8f6f4 v[116:119], v[12:19], v[222:229], v[116:119], v188, v187 op_sel_hi:[0,0,0]
	v_mfma_scale_f32_16x16x128_f8f6f4 v[112:115], v[4:11], v[230:237], v[112:115], v188, v187 op_sel_hi:[0,0,0]
	v_mfma_scale_f32_16x16x128_f8f6f4 v[108:111], v[12:19], v[230:237], v[108:111], v188, v187 op_sel_hi:[0,0,0]
	v_mfma_scale_f32_16x16x128_f8f6f4 v[96:99], v[4:11], v[238:245], v[96:99], v188, v187 op_sel_hi:[0,0,0]
	v_mfma_scale_f32_16x16x128_f8f6f4 v[92:95], v[12:19], v[238:245], v[92:95], v188, v187 op_sel_hi:[0,0,0]
	v_mfma_scale_f32_16x16x128_f8f6f4 v[88:91], v[4:11], v[36:43], v[88:91], v188, v187 op_sel_hi:[0,0,0]
	v_mfma_scale_f32_16x16x128_f8f6f4 v[84:87], v[12:19], v[36:43], v[84:87], v188, v187 op_sel_hi:[0,0,0]
	s_cmp_lg_u32 s23, 6
	s_setprio 0
	s_barrier
	s_cbranch_scc1 .LBB0_1392
	s_mov_b64 s[2:3], -1
	s_cmp_ge_u32 s14, s13
	s_mov_b64 s[10:11], -1
	s_cbranch_scc1 .LBB0_1390

.LBB0_1398:
	s_lshl_b64 s[2:3], s[82:83], 7
	s_add_u32 s26, s6, s2
	v_mov_b32_e32 v2, v186
	v_readfirstlane_b32 s25, v189
	ds_read_b128 v[36:39], v216 offset:16384
	ds_read_b128 v[40:43], v216 offset:17408
	ds_read_b128 v[222:225], v217 offset:16384
	ds_read_b128 v[226:229], v217 offset:17408
	ds_read_b128 v[230:233], v218 offset:16384
	ds_read_b128 v[234:237], v218 offset:17408
	ds_read_b128 v[238:241], v219 offset:16384
	ds_read_b128 v[242:245], v219 offset:17408
	s_addc_u32 s27, s7, s3
	s_mov_b32 m0, s25
	s_add_u32 s28, s26, 0x10000
	global_load_lds_dwordx4 v2, s[26:27]
	v_mov_b32_e32 v2, v186
	v_readfirstlane_b32 s25, v190
	s_addc_u32 s29, s27, 0
	s_mov_b32 m0, s25
	v_readfirstlane_b32 s25, v191
	global_load_lds_dwordx4 v2, s[28:29]
	s_add_u32 s28, s26, 0x20000
	v_mov_b32_e32 v2, v186
	s_addc_u32 s29, s27, 0
	s_mov_b32 m0, s25
	s_add_u32 s26, s26, 0x30000
	global_load_lds_dwordx4 v2, s[28:29]
	v_mov_b32_e32 v2, v186
	v_readfirstlane_b32 s25, v201
	s_addc_u32 s27, s27, 0
	s_mov_b32 m0, s25
	s_add_u32 s2, s4, s2
	global_load_lds_dwordx4 v2, s[26:27]
	v_mov_b32_e32 v2, v182
	v_readfirstlane_b32 s25, v202
	s_addc_u32 s3, s5, s3
	s_mov_b32 m0, s25
	v_readfirstlane_b32 s25, v203
	global_load_lds_dwordx4 v2, s[2:3]
	v_mov_b32_e32 v2, v183
	s_mov_b32 m0, s25
	s_nop 0
	global_load_lds_dwordx4 v2, s[2:3]
	s_waitcnt vmcnt(8)
	s_waitcnt lgkmcnt(0)
	s_setprio 1
	s_barrier
	s_waitcnt lgkmcnt(0)
	v_mfma_scale_f32_16x16x128_f8f6f4 v[144:147], v[20:27], v[36:43], v[144:147], v188, v187 op_sel_hi:[0,0,0]
	v_mfma_scale_f32_16x16x128_f8f6f4 v[140:143], v[28:35], v[36:43], v[140:143], v188, v187 op_sel_hi:[0,0,0]
	v_mfma_scale_f32_16x16x128_f8f6f4 v[136:139], v[20:27], v[222:229], v[136:139], v188, v187 op_sel_hi:[0,0,0]
	v_mfma_scale_f32_16x16x128_f8f6f4 v[132:135], v[28:35], v[222:229], v[132:135], v188, v187 op_sel_hi:[0,0,0]
	v_mfma_scale_f32_16x16x128_f8f6f4 v[128:131], v[20:27], v[230:237], v[128:131], v188, v187 op_sel_hi:[0,0,0]
	v_mfma_scale_f32_16x16x128_f8f6f4 v[124:127], v[28:35], v[230:237], v[124:127], v188, v187 op_sel_hi:[0,0,0]
	v_mfma_scale_f32_16x16x128_f8f6f4 v[100:103], v[20:27], v[238:245], v[100:103], v188, v187 op_sel_hi:[0,0,0]
	v_mfma_scale_f32_16x16x128_f8f6f4 v[104:107], v[28:35], v[238:245], v[104:107], v188, v187 op_sel_hi:[0,0,0]
	s_setprio 0
	s_setprio 1
	v_mfma_scale_f32_16x16x128_f8f6f4 v[80:83], v[4:11], v[36:43], v[80:83], v188, v187 op_sel_hi:[0,0,0]
	v_mfma_scale_f32_16x16x128_f8f6f4 v[76:79], v[12:19], v[36:43], v[76:79], v188, v187 op_sel_hi:[0,0,0]
	v_mfma_scale_f32_16x16x128_f8f6f4 v[72:75], v[4:11], v[222:229], v[72:75], v188, v187 op_sel_hi:[0,0,0]
	v_mfma_scale_f32_16x16x128_f8f6f4 v[68:71], v[12:19], v[222:229], v[68:71], v188, v187 op_sel_hi:[0,0,0]
	v_mfma_scale_f32_16x16x128_f8f6f4 v[64:67], v[4:11], v[230:237], v[64:67], v188, v187 op_sel_hi:[0,0,0]
	v_mfma_scale_f32_16x16x128_f8f6f4 v[60:63], v[12:19], v[230:237], v[60:63], v188, v187 op_sel_hi:[0,0,0]
	v_mfma_scale_f32_16x16x128_f8f6f4 v[52:55], v[4:11], v[238:245], v[52:55], v188, v187 op_sel_hi:[0,0,0]
	v_mfma_scale_f32_16x16x128_f8f6f4 v[56:59], v[12:19], v[238:245], v[56:59], v188, v187 op_sel_hi:[0,0,0]
	s_setprio 0
	s_barrier
	ds_read_b128 v[20:23], v214
	ds_read_b128 v[24:27], v214 offset:1024
	ds_read_b128 v[28:31], v214 offset:2048
	ds_read_b128 v[32:35], v214 offset:3072
	ds_read_b128 v[4:7], v215
	ds_read_b128 v[8:11], v215 offset:1024
	ds_read_b128 v[12:15], v215 offset:2048
	ds_read_b128 v[16:19], v215 offset:3072
	v_mov_b32_e32 v2, v184
	v_readfirstlane_b32 s25, v204
	ds_read_b128 v[36:39], v216 offset:32768
	ds_read_b128 v[40:43], v216 offset:33792
	ds_read_b128 v[222:225], v217 offset:32768
	ds_read_b128 v[226:229], v217 offset:33792
	ds_read_b128 v[230:233], v218 offset:32768
	ds_read_b128 v[234:237], v218 offset:33792
	ds_read_b128 v[238:241], v219 offset:32768
	ds_read_b128 v[242:245], v219 offset:33792
	s_mov_b32 m0, s25
	v_readfirstlane_b32 s25, v205
	global_load_lds_dwordx4 v2, s[2:3]
	v_mov_b32_e32 v2, v185
	s_mov_b32 m0, s25
	s_nop 0
	global_load_lds_dwordx4 v2, s[2:3]
	s_waitcnt vmcnt(8)
	s_waitcnt lgkmcnt(0)
	s_setprio 1
	s_barrier
	s_waitcnt lgkmcnt(0)
	v_mfma_scale_f32_16x16x128_f8f6f4 v[176:179], v[20:27], v[36:43], v[176:179], v188, v187 op_sel_hi:[0,0,0]
	v_mfma_scale_f32_16x16x128_f8f6f4 v[172:175], v[28:35], v[36:43], v[172:175], v188, v187 op_sel_hi:[0,0,0]
	v_mfma_scale_f32_16x16x128_f8f6f4 v[168:171], v[20:27], v[222:229], v[168:171], v188, v187 op_sel_hi:[0,0,0]
	v_mfma_scale_f32_16x16x128_f8f6f4 v[164:167], v[28:35], v[222:229], v[164:167], v188, v187 op_sel_hi:[0,0,0]
	v_mfma_scale_f32_16x16x128_f8f6f4 v[160:163], v[20:27], v[230:237], v[160:163], v188, v187 op_sel_hi:[0,0,0]
	v_mfma_scale_f32_16x16x128_f8f6f4 v[156:159], v[28:35], v[230:237], v[156:159], v188, v187 op_sel_hi:[0,0,0]
	v_mfma_scale_f32_16x16x128_f8f6f4 v[152:155], v[20:27], v[238:245], v[152:155], v188, v187 op_sel_hi:[0,0,0]
	v_mfma_scale_f32_16x16x128_f8f6f4 v[148:151], v[28:35], v[238:245], v[148:151], v188, v187 op_sel_hi:[0,0,0]
	s_setprio 0
	s_setprio 1
	v_mfma_scale_f32_16x16x128_f8f6f4 v[120:123], v[4:11], v[36:43], v[120:123], v188, v187 op_sel_hi:[0,0,0]
	v_mfma_scale_f32_16x16x128_f8f6f4 v[116:119], v[12:19], v[36:43], v[116:119], v188, v187 op_sel_hi:[0,0,0]
	v_mfma_scale_f32_16x16x128_f8f6f4 v[112:115], v[4:11], v[222:229], v[112:115], v188, v187 op_sel_hi:[0,0,0]
	v_mfma_scale_f32_16x16x128_f8f6f4 v[108:111], v[12:19], v[222:229], v[108:111], v188, v187 op_sel_hi:[0,0,0]
	v_mfma_scale_f32_16x16x128_f8f6f4 v[96:99], v[4:11], v[230:237], v[96:99], v188, v187 op_sel_hi:[0,0,0]
	v_mfma_scale_f32_16x16x128_f8f6f4 v[92:95], v[12:19], v[230:237], v[92:95], v188, v187 op_sel_hi:[0,0,0]
	v_mfma_scale_f32_16x16x128_f8f6f4 v[88:91], v[4:11], v[238:245], v[88:91], v188, v187 op_sel_hi:[0,0,0]
	v_mfma_scale_f32_16x16x128_f8f6f4 v[84:87], v[12:19], v[238:245], v[84:87], v188, v187 op_sel_hi:[0,0,0]
	s_setprio 0
	s_barrier
	s_add_i32 s82, s82, 1
	s_lshl_b64 s[2:3], s[82:83], 7
	s_add_u32 s26, s6, s2
	v_mov_b32_e32 v2, v186
	v_readfirstlane_b32 s25, v206
	ds_read_b128 v[36:39], v216 offset:49152
	ds_read_b128 v[40:43], v216 offset:50176
	ds_read_b128 v[222:225], v217 offset:49152
	ds_read_b128 v[226:229], v217 offset:50176
	ds_read_b128 v[230:233], v218 offset:49152
	ds_read_b128 v[234:237], v218 offset:50176
	ds_read_b128 v[238:241], v219 offset:49152
	ds_read_b128 v[242:245], v219 offset:50176
	s_addc_u32 s27, s7, s3
	s_mov_b32 m0, s25
	s_add_u32 s28, s26, 0x10000
	global_load_lds_dwordx4 v2, s[26:27]
	v_mov_b32_e32 v2, v186
	v_readfirstlane_b32 s25, v207
	s_addc_u32 s29, s27, 0
	s_mov_b32 m0, s25
	v_readfirstlane_b32 s25, v210
	global_load_lds_dwordx4 v2, s[28:29]
	s_add_u32 s28, s26, 0x20000
	v_mov_b32_e32 v2, v186
	s_addc_u32 s29, s27, 0
	s_mov_b32 m0, s25
	s_add_u32 s26, s26, 0x30000
	global_load_lds_dwordx4 v2, s[28:29]
	v_mov_b32_e32 v2, v186
	v_readfirstlane_b32 s25, v211
	s_addc_u32 s27, s27, 0
	s_mov_b32 m0, s25
	s_add_u32 s2, s4, s2
	global_load_lds_dwordx4 v2, s[26:27]
	v_mov_b32_e32 v2, v182
	v_readfirstlane_b32 s25, v208
	s_addc_u32 s3, s5, s3
	s_mov_b32 m0, s25
	v_readfirstlane_b32 s25, v209
	global_load_lds_dwordx4 v2, s[2:3]
	v_mov_b32_e32 v2, v183
	s_mov_b32 m0, s25
	s_nop 0
	global_load_lds_dwordx4 v2, s[2:3]
	s_waitcnt vmcnt(8)
	s_waitcnt lgkmcnt(0)
	s_setprio 1
	s_barrier
	s_waitcnt lgkmcnt(0)
	v_mfma_scale_f32_16x16x128_f8f6f4 v[144:147], v[20:27], v[36:43], v[144:147], v188, v187 op_sel_hi:[0,0,0]
	v_mfma_scale_f32_16x16x128_f8f6f4 v[140:143], v[28:35], v[36:43], v[140:143], v188, v187 op_sel_hi:[0,0,0]
	v_mfma_scale_f32_16x16x128_f8f6f4 v[136:139], v[20:27], v[222:229], v[136:139], v188, v187 op_sel_hi:[0,0,0]
	v_mfma_scale_f32_16x16x128_f8f6f4 v[132:135], v[28:35], v[222:229], v[132:135], v188, v187 op_sel_hi:[0,0,0]
	v_mfma_scale_f32_16x16x128_f8f6f4 v[128:131], v[20:27], v[230:237], v[128:131], v188, v187 op_sel_hi:[0,0,0]
	v_mfma_scale_f32_16x16x128_f8f6f4 v[124:127], v[28:35], v[230:237], v[124:127], v188, v187 op_sel_hi:[0,0,0]
	v_mfma_scale_f32_16x16x128_f8f6f4 v[100:103], v[20:27], v[238:245], v[100:103], v188, v187 op_sel_hi:[0,0,0]
	v_mfma_scale_f32_16x16x128_f8f6f4 v[104:107], v[28:35], v[238:245], v[104:107], v188, v187 op_sel_hi:[0,0,0]
	s_setprio 0
	s_setprio 1
	v_mfma_scale_f32_16x16x128_f8f6f4 v[80:83], v[4:11], v[36:43], v[80:83], v188, v187 op_sel_hi:[0,0,0]
	v_mfma_scale_f32_16x16x128_f8f6f4 v[76:79], v[12:19], v[36:43], v[76:79], v188, v187 op_sel_hi:[0,0,0]
	v_mfma_scale_f32_16x16x128_f8f6f4 v[72:75], v[4:11], v[222:229], v[72:75], v188, v187 op_sel_hi:[0,0,0]
	v_mfma_scale_f32_16x16x128_f8f6f4 v[68:71], v[12:19], v[222:229], v[68:71], v188, v187 op_sel_hi:[0,0,0]
	v_mfma_scale_f32_16x16x128_f8f6f4 v[64:67], v[4:11], v[230:237], v[64:67], v188, v187 op_sel_hi:[0,0,0]
	v_mfma_scale_f32_16x16x128_f8f6f4 v[60:63], v[12:19], v[230:237], v[60:63], v188, v187 op_sel_hi:[0,0,0]
	v_mfma_scale_f32_16x16x128_f8f6f4 v[52:55], v[4:11], v[238:245], v[52:55], v188, v187 op_sel_hi:[0,0,0]
	v_mfma_scale_f32_16x16x128_f8f6f4 v[56:59], v[12:19], v[238:245], v[56:59], v188, v187 op_sel_hi:[0,0,0]
	s_setprio 0
	s_barrier
	s_cmp_gt_u32 s23, 5
	s_cbranch_scc1 .LBB0_1400
	s_mov_b32 s23, s24
	s_branch .LBB0_1387
